# HGRN filler load step: slot-linear scalar base + per-lane offset from tid (no per-step descriptor decode), on top of v55
# baseline (speedup 1.0000x reference)
; DEV int ltid() { int t = threadIdx.x; asm volatile("" : "+v"(t)); return t; }
; DEV FillDesc fill_decode(CParams& p, int wg, int slot) {
;   const int h = slot * 256 + wg, t = h >> 1, half = h & 1; FillDesc d;
;   if (t < NE * 512) { const int e = t >> 9, r = t & 511; d.src = p.w_gu + (long)e * 2048 * 4096; d.ldsrc = 4096; d.dst = p.wt_gu8 + (long)e * 4096 * 2048; d.perm = 2; d.n0 = (r & 31) * 128 + 64 * half; d.kh = (r >> 5) * 128; }
;   else { const int v = t - NE * 512, e = v >> 8, r = v & 255; d.src = p.w_dn + (long)e * 2048 * 2048; d.ldsrc = 2048; d.dst = p.wt_dn8 + (long)e * 2048 * 2048; d.perm = 0; d.n0 = (r & 15) * 128 + 64 * half; d.kh = (r >> 4) * 128; }
;   return d;
; }
; DEV void fill_load(CParams& p, int wg, int slot, f32x4 (&ld)[4]) {
;   const FillDesc d = fill_decode(p, wg, slot); const int tid = ltid(), tx = tid & 15, ty = tid >> 4;
;   const float* sp = d.src + (long)(d.kh + 4 * ty) * d.ldsrc + d.n0 + 4 * tx;
; #pragma unroll
;   for (int r = 0; r < 4; ++r) ld[r] = *(const f32x4*)(sp + (long)r * d.ldsrc);
; }
; DEV void hgrn_unit(CParams& p, int u, int wg, bool fill) {
;     ...
;   f32x4 fldA[4], fldB[4];
;   if (fill && FILL_HG > 0) { fill_load(p, wg, 0, fldA); if (FILL_HG > 1) fill_load(p, wg, 1, fldB); }
;   HG_LOAD(0, g, q, v);
;   HG_ELEM(0, false);
;   HG_LOAD(1, g, q, v);
;   __syncthreads();
;   HG_STEP(0, false, false, fldA); HG_STEP(1, false, false, fldB); HG_STEP(2, false, false, fldA);
.LBB0_766:
	v_or_b32_e32 v18, v108, v109
	v_mov_b32_e32 v22, v0
	v_add_u32_e32 v194, v18, v116
	v_add_u32_e32 v195, v18, v110
	s_lshl_b32 s21, s24, s21
	s_lshl_b32 s22, s24, 7
	v_ashrrev_i32_e32 v18, 2, v22
	s_and_b32 s21, s21, 0x780
	v_and_b32_e32 v18, -4, v18
	s_and_b32 s22, s22, 0x780
	v_add_u32_e32 v18, s21, v18
	s_or_b32 s25, s22, s3
	v_mad_i64_i32 v[18:19], s[22:23], s20, v18, 0
	v_lshl_add_u64 v[18:19], v[18:19], 2, s[18:19]
	s_lshl_b32 s62, s25, 2
	s_mov_b32 s63, 0
	v_lshl_add_u64 v[20:21], v[18:19], 0, s[62:63]
	v_lshlrev_b32_e32 v18, 4, v22
	v_and_b32_e32 v18, 0xf0, v18
	v_mov_b32_e32 v19, 0
	v_lshl_add_u64 v[20:21], v[20:21], 0, v[18:19]
	s_lshl_b32 s62, s20, 2
	v_lshl_add_u64 v[30:31], v[20:21], 0, s[62:63]
	global_load_dwordx4 v[22:25], v[20:21], off
	global_load_dwordx4 v[26:29], v[30:31], off
	v_lshl_add_u64 v[20:21], v[30:31], 0, s[62:63]
	s_waitcnt lgkmcnt(12)
	v_cndmask_b32_e64 v130, v36, v35, s[12:13]
	v_lshl_add_u64 v[48:49], v[20:21], 0, s[62:63]
	global_load_dwordx4 v[30:33], v[20:21], off
	global_load_dwordx4 v[34:37], v[48:49], off
	s_add_u32 s16, s16, s56
	s_addc_u32 s17, s17, 0
	s_add_u32 s16, s16, s60
	s_addc_u32 s17, s17, 0
	v_mov_b32_e32 v59, v19
	v_lshl_add_u64 v[108:109], s[16:17], 0, v[58:59]
	s_add_u32 s16, s58, s56
	s_addc_u32 s17, s59, 0
	v_ashrrev_i32_e32 v48, 7, v112
	s_add_u32 s16, s16, s60
	v_lshl_or_b32 v18, v48, 4, v113
	s_movk_i32 s62, 0x110
	v_and_b32_e32 v106, 16, v106
	s_addc_u32 s17, s17, 0
	v_mul_lo_u32 v49, v18, s62
	v_lshlrev_b32_e32 v52, 1, v18
	v_mul_lo_u32 v103, v18, s36
	v_lshlrev_b32_e32 v18, 1, v106
	v_or_b32_e32 v47, 3, v102
	v_lshl_add_u64 v[20:21], s[16:17], 0, v[18:19]
	v_lshlrev_b32_e32 v18, 1, v102
	s_add_i32 s16, 0, 0x1e600
	s_add_i32 s61, 0, 0x10400
	s_waitcnt lgkmcnt(0)
	s_barrier
	s_load_dwordx4 s[44:47], s[14:15], 0xe8
	v_add_u32_e32 v202, 0, v49
	v_lshl_add_u64 v[110:111], v[20:21], 0, v[18:19]
	v_add3_u32 v204, s16, v51, v46
	s_load_dwordx2 s[64:65], s[14:15], 0xa0
	s_load_dwordx2 s[66:67], s[14:15], 0xb0
	v_add_u32_e32 v205, s61, v49
	v_or_b32_e32 v21, 64, v114
	v_or_b32_e32 v49, 0x80, v114
	v_or_b32_e32 v51, 0xc0, v114
	v_cmp_gt_u32_e64 s[24:25], v47, v113
	v_or_b32_e32 v47, 32, v46
	s_movk_i32 s26, 0x70
	v_bitop3_b32 v183, v46, v114, 16 bitop3:0x6c
	v_bitop3_b32 v182, v46, v21, 16 bitop3:0x6c
	v_bitop3_b32 v181, v46, v49, 16 bitop3:0x6c
	v_bitop3_b32 v180, v46, v51, 16 bitop3:0x6c
	v_bitop3_b32 v178, v47, v114, 48 bitop3:0x6c
	v_bitop3_b32 v177, v47, v21, 48 bitop3:0x6c
	v_bitop3_b32 v176, v47, v49, 48 bitop3:0x6c
	v_bitop3_b32 v175, v47, v51, 48 bitop3:0x6c
	v_or_b32_e32 v47, 64, v46
	s_movk_i32 s27, 0x50
	v_or_b32_e32 v46, 0x60, v46
	v_or_b32_e32 v53, v106, v113
	v_bitop3_b32 v207, v52, v21, s26 bitop3:0x6c
	v_bitop3_b32 v172, v47, v21, s27 bitop3:0x6c
	v_bitop3_b32 v165, v46, v21, s26 bitop3:0x6c
	v_mov_b32_e32 v21, s80
	v_mul_u32_u24_e32 v203, 0x110, v53
	v_mul_u32_u24_e32 v18, 0x48, v53
	v_add_u32_e32 v20, s16, v114
	s_movk_i32 s14, 0x80
	v_mad_u32_u24 v191, v113, s62, 0
	v_mad_u32_u24 v184, v113, s62, v21
	v_mul_u32_u24_e32 v192, 0x440, v70
	v_mul_u32_u24_e32 v193, 0x110, v50
	v_add_u32_e32 v196, 0x220, v194
	v_add_u32_e32 v197, 0x330, v194
	v_add_u32_e32 v198, 0x440, v194
	v_add_u32_e32 v199, 0x550, v194
	v_add_u32_e32 v200, 0x660, v194
	v_add_u32_e32 v201, 0x770, v194
	s_mov_b32 s57, 4
	v_mul_u32_u24_e32 v187, 0x90, v53
	v_lshl_add_u32 v188, v70, 3, 0
	v_add_u32_e32 v186, 0xfffffc00, v103
	v_bitop3_b32 v206, v52, v114, s26 bitop3:0x6c
	v_bitop3_b32 v208, v52, v49, s26 bitop3:0x6c
	v_bitop3_b32 v209, v52, v51, s26 bitop3:0x6c
	v_cmp_lt_i32_e64 s[16:17], -1, v48
	v_cmp_gt_u32_e64 s[38:39], s14, v112
	v_cmp_gt_u32_e64 s[18:19], v102, v113
	v_cmp_lt_u32_e64 s[20:21], v102, v113
	v_cmp_gt_u32_e64 s[22:23], v50, v113
	v_cmp_lt_i32_e64 s[36:37], 0, v48
	v_add_u32_e32 v190, 0x1100, v191
	v_cmp_eq_u32_e64 s[34:35], 1, v48
	v_cmp_lt_i32_e64 s[14:15], 1, v48
	v_add_u32_e32 v189, 0x2200, v191
	v_bitop3_b32 v173, v47, v114, s27 bitop3:0x6c
	v_bitop3_b32 v171, v47, v49, s27 bitop3:0x6c
	v_bitop3_b32 v170, v47, v51, s27 bitop3:0x6c
	v_cmp_eq_u32_e64 s[30:31], 2, v48
	v_cmp_lt_i32_e64 s[28:29], 2, v48
	v_bitop3_b32 v167, v46, v114, s26 bitop3:0x6c
	v_bitop3_b32 v164, v46, v49, s26 bitop3:0x6c
	v_bitop3_b32 v163, v46, v51, s26 bitop3:0x6c
	v_cmp_eq_u32_e64 s[26:27], 3, v48
	v_add_u32_e32 v179, 0x1100, v184
	v_add_u32_e32 v174, 0x2200, v184
	v_add_u32_e32 v166, 0x3300, v184
	v_add_lshl_u32 v210, v18, v102, 1
	s_add_i32 s82, s2, 0x700
	s_movk_i32 s83, 0x84
	s_movk_i32 s84, 0x7ff
	s_mov_b32 s85, 0xda24260
	v_mov_b32_e32 v211, 0xfffff800
	v_mov_b32_e32 v212, 0x80
	v_mov_b32_e32 v213, 0x7149f2ca
	v_add_u32_e32 v160, v20, v203
	s_mov_b32 s86, 0
	s_mov_b32 s87, 0
	v_readfirstlane_b32 s32, v82
	v_readfirstlane_b32 s92, v83
	v_readfirstlane_b32 s93, v84
	v_readfirstlane_b32 s94, v85
	v_readfirstlane_b32 s95, v108
	v_readfirstlane_b32 s96, v109
	s_nop 1
	v_subrev_u32_e32 v82, s32, v82
	v_add_u32_e32 v82, 0x40000, v82
	v_subrev_u32_e32 v108, s95, v108
	v_add_u32_e32 v108, 0x20000, v108
	v_lshl_add_u32 v151, v151, 12, v82
	v_lshl_add_u32 v135, v135, 12, v82
	v_lshl_add_u32 v136, v136, 12, v82
	v_lshl_add_u32 v137, v137, 12, v82
	v_lshl_add_u32 v138, v138, 12, v82
	v_lshl_add_u32 v139, v139, 12, v82
	v_lshl_add_u32 v141, v141, 12, v82
	v_lshl_add_u32 v143, v143, 12, v82
	v_lshl_add_u32 v144, v144, 11, v108
	s_waitcnt lgkmcnt(0)
	s_lshr_b32 s70, s2, 1
	s_and_b32 s71, s70, 31
	s_lshl_b32 s71, s71, 7
	s_or_b32 s71, s71, s3
	s_lshr_b32 s72, s70, 5
	s_lshl_b32 s72, s72, 7
	v_lshrrev_b32_e32 v20, 3, v0
	v_and_b32_e32 v21, 7, v0
	v_lshlrev_b32_e32 v21, 4, v21
	v_mul_u32_u24_e32 v212, 0x84, v20
	v_add_u32_e32 v212, v212, v21
	v_add_u32_e32 v211, s71, v20
	v_and_b32_e32 v46, 0x7ff, v211
	v_lshrrev_b32_e32 v211, 11, v211
	v_lshlrev_b32_e32 v211, 7, v211
	v_and_b32_e32 v47, 0x7f, v46
	v_or_b32_e32 v211, v211, v47
	v_lshrrev_b32_e32 v46, 7, v46
	v_lshl_or_b32 v211, v46, 8, v211
	v_lshlrev_b32_e32 v211, 11, v211
	v_add_u32_e32 v211, v211, v21
	v_add_u32_e32 v211, s72, v211
	s_lshl_b32 s98, s72, 14
	s_lshl_b32 s73, s71, 2
	s_add_u32 s98, s98, s73
	s_branch .LBB0_770

.LBB0_796:
	s_or_b64 exec, exec, s[68:69]
	v_add_u32_e32 v217, v149, v203
	ds_read_b128 v[62:65], v217 offset:57856
	ds_read_b128 v[66:69], v217 offset:57920
	ds_read_b128 v[70:73], v142 offset:34816
	ds_read_b128 v[74:77], v142 offset:34880
	ds_read_b128 v[224:227], v217 offset:57984
	s_add_i32 s62, s88, 0x13ff
	s_add_i32 s70, s89, 0x400
	v_pk_mul_f32 v[44:45], v[44:45], v[130:131] op_sel_hi:[1,0]
	v_pk_mul_f32 v[42:43], v[42:43], v[130:131] op_sel_hi:[1,0]
	s_and_b64 s[68:69], s[52:53], exec
	s_cselect_b32 s62, s70, s62
	s_waitcnt lgkmcnt(4)
	v_mfma_f32_16x16x32_bf16 v[58:61], v[62:65], v[58:61], v[78:81]
	ds_read_b128 v[62:65], v154 offset:53248
	s_nop 1
	ds_read_b128 v[78:81], v217 offset:58048
	v_add_u32_e32 v20, s62, v186
	v_ashrrev_i32_e32 v21, 31, v20
	s_waitcnt lgkmcnt(5)
	v_mfma_f32_16x16x32_bf16 v[50:53], v[66:69], v[50:53], v[58:61]
	v_lshlrev_b64 v[20:21], 11, v[20:21]
	v_pk_mul_f32 v[40:41], v[40:41], v[130:131] op_sel_hi:[1,0]
	v_pk_mul_f32 v[38:39], v[38:39], v[130:131] op_sel_hi:[1,0]
	s_waitcnt lgkmcnt(2)
	v_mfma_f32_16x16x32_bf16 v[50:53], v[224:227], v[54:57], v[50:53]
	s_waitcnt vmcnt(33)
	v_pk_mul_f32 v[60:61], v[98:99], v[100:101]
	ds_read_b128 v[54:57], v154 offset:53312
	v_lshl_add_u64 v[58:59], v[110:111], 0, v[20:21]
	s_waitcnt lgkmcnt(1)
	v_mfma_f32_16x16x32_bf16 v[48:51], v[78:81], v[46:49], v[50:53]
	v_add_u32_e32 v214, v204, v192
	v_add_u32_e32 v218, v204, v193
	v_add_u32_e32 v221, s80, v194
	v_mfma_f32_16x16x32_bf16 v[42:45], v[62:65], v[70:73], v[42:45]
	s_waitcnt vmcnt(31)
	v_pk_mul_f32 v[62:63], v[96:97], v[60:61]
	s_nop 1
	v_cvt_pk_bf16_f32 v52, v48, v49
	s_waitcnt vmcnt(29)
	v_pk_mul_f32 v[64:65], v[94:95], v[62:63]
	v_cvt_pk_bf16_f32 v53, v50, v51
	s_waitcnt vmcnt(27)
	v_pk_mul_f32 v[66:67], v[92:93], v[64:65]
	global_store_dwordx2 v[58:59], v[52:53], off
	s_waitcnt vmcnt(26)
	v_pk_mul_f32 v[48:49], v[90:91], v[66:67]
	ds_read_b128 v[50:53], v154 offset:55552
	s_waitcnt vmcnt(24)
	v_pk_mul_f32 v[46:47], v[88:89], v[48:49]
	s_waitcnt lgkmcnt(1)
	v_mfma_f32_16x16x32_bf16 v[42:45], v[54:57], v[74:77], v[42:45]
	s_waitcnt vmcnt(22)
	v_pk_mul_f32 v[20:21], v[86:87], v[46:47]
	ds_bpermute_b32 v68, v1, v20
	ds_bpermute_b32 v69, v1, v21
	s_waitcnt lgkmcnt(2)
	v_mfma_f32_16x16x32_bf16 v[38:41], v[50:53], v[70:73], v[38:41]
	s_waitcnt lgkmcnt(0)
	v_pk_mul_f32 v[54:55], v[20:21], v[68:69]
	v_add_u32_e32 v222, s61, v194
	v_cndmask_b32_e64 v59, v55, v21, s[6:7]
	v_cndmask_b32_e64 v58, v54, v20, s[6:7]
	ds_bpermute_b32 v68, v107, v58
	ds_bpermute_b32 v69, v107, v59
	ds_read_b128 v[54:57], v154 offset:55616
	s_waitcnt lgkmcnt(0)
	v_mfma_f32_16x16x32_bf16 v[38:41], v[54:57], v[74:77], v[38:41]
	v_mul_f32_e64 v50, v58, v68
	v_mul_f32_e64 v51, v59, v69
	s_waitcnt vmcnt(21)
	ds_write_b16 v140, v104
	ds_write_b16_d16_hi v140, v104 offset:144
	ds_write_b16 v140, v105 offset:288
	v_cndmask_b32_e64 v51, v51, v59, s[8:9]
	v_cndmask_b32_e64 v50, v50, v58, s[8:9]
	ds_bpermute_b32 v52, v131, v50
	ds_bpermute_b32 v53, v131, v51
	ds_write_b16_d16_hi v140, v105 offset:432
	v_add_u32_e32 v224, s80, v195
	v_add_u32_e32 v225, s61, v195
	v_add_u32_e32 v226, s80, v196
	s_waitcnt lgkmcnt(1)
	v_pk_mul_f32 v[52:53], v[50:51], v[52:53]
	v_add_u32_e32 v227, s61, v196
	v_cndmask_b32_e64 v18, v52, v50, s[10:11]
	ds_bpermute_b32 v50, v1, v18
	v_cndmask_b32_e64 v51, v53, v51, s[10:11]
	ds_bpermute_b32 v53, v150, v18
	ds_bpermute_b32 v52, v1, v51
	ds_bpermute_b32 v54, v148, v51
	s_waitcnt lgkmcnt(3)
	v_cndmask_b32_e64 v59, 1.0, v50, s[4:5]
	ds_bpermute_b32 v50, v148, v18
	ds_bpermute_b32 v18, v150, v51
	s_waitcnt lgkmcnt(4)
	v_max_f32_e32 v51, v53, v53
	v_max_f32_e32 v51, 0x554ad2e, v51
	v_rcp_f32_e32 v68, v51
	ds_bpermute_b32 v51, v132, v53
	s_waitcnt lgkmcnt(1)
	ds_bpermute_b32 v53, v132, v18
	v_max_f32_e32 v18, v18, v18
	v_max_f32_e32 v55, 0x554ad2e, v18
	v_mul_f32_e32 v18, v68, v50
	ds_bpermute_b32 v130, v132, v50
	s_waitcnt lgkmcnt(1)
	v_cndmask_b32_e64 v50, v53, v51, s[12:13]
	v_mul_f32_e32 v51, v42, v50
	v_cvt_pk_bf16_f32 v51, v51, s0
	ds_write_b16 v214, v51
	v_mul_f32_e32 v51, v43, v50
	v_cvt_pk_bf16_f32 v51, v51, s0
	ds_write_b16 v214, v51 offset:272
	v_mul_f32_e32 v51, v44, v50
	v_cvt_pk_bf16_f32 v51, v51, s0
	ds_write_b16 v218, v51
	v_mul_f32_e32 v51, v45, v50
	v_cvt_pk_bf16_f32 v51, v51, s0
	ds_write_b16 v218, v51 offset:272
	v_mul_f32_e32 v51, v38, v50
	v_cvt_pk_bf16_f32 v51, v51, s0
	ds_write_b16 v214, v51 offset:4352
	v_mul_f32_e32 v51, v39, v50
	v_cvt_pk_bf16_f32 v51, v51, s0
	v_rcp_f32_e32 v70, v55
	ds_write_b16 v214, v51 offset:4624
	v_mul_f32_e32 v51, v40, v50
	v_mul_f32_e32 v50, v41, v50
	v_cvt_pk_bf16_f32 v51, v51, s0
	v_cvt_pk_bf16_f32 v50, v50, s0
	v_cndmask_b32_e64 v69, 1.0, v52, s[4:5]
	ds_write_b16 v214, v51 offset:4896
	ds_write_b16 v214, v50 offset:5168
	v_mul_f32_e32 v50, v100, v59
	v_mul_f32_e32 v51, v101, v69
	v_mul_f32_e32 v50, v50, v68
	v_mul_f32_e32 v51, v51, v70
	v_med3_f32 v50, v50, s85, v213
	v_med3_f32 v51, v51, s85, v213
	v_rcp_f32_e32 v52, v50
	v_rcp_f32_e32 v53, v51
	v_mul_f32_e32 v58, v70, v54
	ds_bpermute_b32 v251, v132, v54
	v_pk_add_f32 v[54:55], v[100:101], 1.0 op_sel_hi:[1,0] neg_lo:[1,0] neg_hi:[1,0]
	v_add_u32_e32 v228, s80, v197
	v_pk_mul_f32 v[52:53], v[54:55], v[52:53]
	v_and_b32_e32 v55, 0xffff0000, v169
	v_cvt_pk_bf16_f32 v54, v52, v53
	ds_write_b32 v221, v54
	v_lshlrev_b32_e32 v54, 16, v169
	v_pk_mul_f32 v[50:51], v[50:51], v[54:55]
	v_add_u32_e32 v229, s61, v197
	v_cvt_pk_bf16_f32 v56, v50, v51
	v_mul_f32_e32 v50, v60, v59
	v_mul_f32_e32 v51, v61, v69
	v_mul_f32_e32 v50, v50, v68
	v_mul_f32_e32 v51, v51, v70
	v_med3_f32 v50, v50, s85, v213
	v_med3_f32 v51, v51, s85, v213
	v_rcp_f32_e32 v54, v50
; DEV int ltid() { int t = threadIdx.x; asm volatile("" : "+v"(t)); return t; }
; DEV unsigned cvt_pk4_fp8(f32x4 v) { unsigned r = 0; r = __builtin_amdgcn_cvt_pk_fp8_f32(v[0], v[1], r, false); r = __builtin_amdgcn_cvt_pk_fp8_f32(v[2], v[3], r, true); return r; }
; DEV void fill_write(const f32x4 (&ld)[4], int bufsel) {
;   extern __shared__ __attribute__((aligned(16))) char shm[];
;   unsigned* T = (unsigned*)(shm + FILL_LDS_OFF + bufsel * FILL_TB); const int tid = ltid(), tx = tid & 15, ty = tid >> 4;
;   constexpr float WS = (float)(1 << FP8_WSCALE_LOG2_);
; #pragma unroll
;   for (int j = 0; j < 4; ++j) T[(4 * tx + j) * 33 + ty] = cvt_pk4_fp8((f32x4){ld[0][j] * WS, ld[1][j] * WS, ld[2][j] * WS, ld[3][j] * WS});
; }
	v_rcp_f32_e32 v55, v51
	ds_write_b32 v222, v56
	v_pk_add_f32 v[56:57], v[98:99], 1.0 op_sel_hi:[1,0] neg_lo:[1,0] neg_hi:[1,0]
	v_add_u32_e32 v230, s80, v198
	v_pk_mul_f32 v[54:55], v[56:57], v[54:55]
	v_and_b32_e32 v57, 0xffff0000, v168
	v_cvt_pk_bf16_f32 v56, v54, v55
	ds_write_b32 v224, v56
	v_lshlrev_b32_e32 v56, 16, v168
	v_pk_mul_f32 v[50:51], v[50:51], v[56:57]
	v_mul_f32_e32 v48, v48, v59
	v_cvt_pk_bf16_f32 v50, v50, v51
	v_mov_b32_e32 v51, v54
	v_mov_b32_e32 v54, v53
	ds_write_b32 v225, v50
	v_mov_b32_e32 v50, v52
	v_pk_mul_f32 v[52:53], v[58:59], v[54:55] op_sel_hi:[0,1]
	v_mul_f32_e32 v54, v62, v59
	v_mul_f32_e32 v54, v54, v68
	v_med3_f32 v56, v54, s85, v213
	v_mul_f32_e32 v54, v63, v69
	v_mul_f32_e32 v54, v54, v70
	v_med3_f32 v57, v54, s85, v213
	v_rcp_f32_e32 v60, v56
	v_rcp_f32_e32 v61, v57
	v_cvt_pk_bf16_f32 v54, v52, v53
	v_pk_add_f32 v[52:53], v[96:97], 1.0 op_sel_hi:[1,0] neg_lo:[1,0] neg_hi:[1,0]
	v_pk_mul_f32 v[50:51], v[18:19], v[50:51] op_sel_hi:[0,1]
	v_pk_mul_f32 v[52:53], v[52:53], v[60:61]
	v_lshlrev_b32_e32 v60, 16, v162
	v_and_b32_e32 v61, 0xffff0000, v162
	v_mul_f32_e32 v55, v64, v59
	v_cvt_pk_bf16_f32 v50, v50, v51
	v_cvt_pk_bf16_f32 v51, v52, v53
	v_pk_mul_f32 v[56:57], v[56:57], v[60:61]
	v_mul_f32_e32 v55, v55, v68
	ds_write_b32 v226, v51
	v_cvt_pk_bf16_f32 v51, v56, v57
	v_med3_f32 v56, v55, s85, v213
	v_mul_f32_e32 v55, v65, v69
	v_mul_f32_e32 v55, v55, v70
	v_med3_f32 v57, v55, s85, v213
	v_rcp_f32_e32 v60, v56
	v_rcp_f32_e32 v61, v57
	v_pk_add_f32 v[62:63], v[94:95], 1.0 op_sel_hi:[1,0] neg_lo:[1,0] neg_hi:[1,0]
	ds_write_b32 v227, v51
	v_mul_f32_e32 v49, v49, v69
	v_pk_mul_f32 v[60:61], v[62:63], v[60:61]
	v_lshlrev_b32_e32 v62, 16, v161
	v_and_b32_e32 v63, 0xffff0000, v161
	v_cvt_pk_bf16_f32 v51, v60, v61
	v_pk_mul_f32 v[56:57], v[56:57], v[62:63]
	ds_write_b32 v228, v51
	v_cvt_pk_bf16_f32 v51, v56, v57
	ds_write_b32 v229, v51
	v_mul_f32_e32 v51, v66, v59
	v_mov_b32_e32 v57, v60
	v_mov_b32_e32 v60, v53
	v_mul_f32_e32 v51, v51, v68
	v_mov_b32_e32 v56, v52
	v_pk_mul_f32 v[52:53], v[58:59], v[60:61] op_sel_hi:[0,1]
	v_med3_f32 v60, v51, s85, v213
	v_mul_f32_e32 v51, v67, v69
	v_mul_f32_e32 v51, v51, v70
	v_med3_f32 v61, v51, s85, v213
	v_rcp_f32_e32 v62, v60
	v_rcp_f32_e32 v63, v61
	v_cvt_pk_bf16_f32 v55, v52, v53
	v_pk_add_f32 v[52:53], v[92:93], 1.0 op_sel_hi:[1,0] neg_lo:[1,0] neg_hi:[1,0]
	v_pk_mul_f32 v[56:57], v[18:19], v[56:57] op_sel_hi:[0,1]
	v_pk_mul_f32 v[52:53], v[52:53], v[62:63]
	v_cvt_pk_bf16_f32 v51, v56, v57
	v_cvt_pk_bf16_f32 v56, v52, v53
	ds_write_b32 v230, v56
	v_lshlrev_b32_e32 v56, 16, v159
	v_and_b32_e32 v57, 0xffff0000, v159
	v_mul_f32_e32 v48, v48, v68
	v_mul_f32_e32 v49, v49, v70
	v_pk_mul_f32 v[56:57], v[60:61], v[56:57]
	v_med3_f32 v48, v48, s85, v213
	v_med3_f32 v49, v49, s85, v213
	v_cvt_pk_bf16_f32 v60, v56, v57
	v_rcp_f32_e32 v56, v48
	v_rcp_f32_e32 v57, v49
	v_add_u32_e32 v231, s61, v198
	ds_write_b32 v231, v60
	v_pk_add_f32 v[60:61], v[90:91], 1.0 op_sel_hi:[1,0] neg_lo:[1,0] neg_hi:[1,0]
	v_add_u32_e32 v232, s80, v199
	v_pk_mul_f32 v[56:57], v[60:61], v[56:57]
	v_mul_f32_e32 v46, v46, v59
	v_cvt_pk_bf16_f32 v60, v56, v57
	v_mul_f32_e32 v47, v47, v69
	ds_write_b32 v232, v60
	v_lshlrev_b32_e32 v60, 16, v158
	v_and_b32_e32 v61, 0xffff0000, v158
	v_mul_f32_e32 v46, v46, v68
	v_mul_f32_e32 v47, v47, v70
	v_pk_mul_f32 v[48:49], v[48:49], v[60:61]
	v_med3_f32 v46, v46, s85, v213
	v_med3_f32 v47, v47, s85, v213
	v_cvt_pk_bf16_f32 v48, v48, v49
	v_add_u32_e32 v233, s61, v199
	v_rcp_f32_e32 v60, v46
	v_rcp_f32_e32 v61, v47
	ds_write_b32 v233, v48
	v_mov_b32_e32 v48, v52
	v_mov_b32_e32 v49, v56
	v_pk_mul_f32 v[48:49], v[18:19], v[48:49] op_sel_hi:[0,1]
	v_cvt_pk_bf16_f32 v52, v48, v49
	v_pk_add_f32 v[48:49], v[88:89], 1.0 op_sel_hi:[1,0] neg_lo:[1,0] neg_hi:[1,0]
	v_mul_f32_e32 v20, v20, v59
	v_mul_f32_e32 v21, v21, v69
	v_pk_mul_f32 v[48:49], v[48:49], v[60:61]
	v_lshlrev_b32_e32 v60, 16, v157
	v_and_b32_e32 v61, 0xffff0000, v157
	v_mul_f32_e32 v20, v20, v68
	v_mul_f32_e32 v21, v21, v70
	v_mov_b32_e32 v56, v53
	v_cvt_pk_bf16_f32 v53, v48, v49
	v_add_u32_e32 v234, s80, v200
	v_pk_mul_f32 v[46:47], v[46:47], v[60:61]
	v_med3_f32 v20, v20, s85, v213
	v_med3_f32 v21, v21, s85, v213
	ds_write_b32 v234, v53
	v_cvt_pk_bf16_f32 v53, v46, v47
	v_rcp_f32_e32 v46, v20
	v_rcp_f32_e32 v47, v21
	v_pk_add_f32 v[60:61], v[86:87], 1.0 op_sel_hi:[1,0] neg_lo:[1,0] neg_hi:[1,0]
	v_add_u32_e32 v235, s61, v200
	v_add_u32_e32 v237, s61, v201
	v_pk_mul_f32 v[46:47], v[60:61], v[46:47]
	v_lshlrev_b32_e32 v60, 16, v156
	v_and_b32_e32 v61, 0xffff0000, v156
	v_pk_mul_f32 v[20:21], v[20:21], v[60:61]
	ds_write_b32 v235, v53
	v_cvt_pk_bf16_f32 v20, v20, v21
	ds_write_b32 v237, v20
	v_mov_b32_e32 v20, v48
	v_mov_b32_e32 v21, v46
	v_cvt_pk_bf16_f32 v53, v46, v47
	v_add_u32_e32 v236, s80, v201
	v_pk_mul_f32 v[20:21], v[18:19], v[20:21] op_sel_hi:[0,1]
	ds_write_b32 v236, v53
	v_cvt_pk_bf16_f32 v53, v20, v21
	v_mul_f32_e32 v10, 0x42800000, v10
	v_mul_f32_e32 v14, 0x42800000, v14
	v_mov_b32_e32 v21, v19
	v_cvt_pk_fp8_f32 v21, v10, v14
	v_mul_f32_e32 v10, 0x42800000, v11
; DEV int ltid() { int t = threadIdx.x; asm volatile("" : "+v"(t)); return t; }
; DEV unsigned cvt_pk4_fp8(f32x4 v) { unsigned r = 0; r = __builtin_amdgcn_cvt_pk_fp8_f32(v[0], v[1], r, false); r = __builtin_amdgcn_cvt_pk_fp8_f32(v[2], v[3], r, true); return r; }
; DEV void fill_load(CParams& p, int wg, int slot, f32x4 (&ld)[4]) {
;   const FillDesc d = fill_decode(p, wg, slot); const int tid = ltid(), tx = tid & 15, ty = tid >> 4;
;   const float* sp = d.src + (long)(d.kh + 4 * ty) * d.ldsrc + d.n0 + 4 * tx;
; #pragma unroll
;   for (int r = 0; r < 4; ++r) ld[r] = *(const f32x4*)(sp + (long)r * d.ldsrc);
; }
; DEV void fill_write(const f32x4 (&ld)[4], int bufsel) {
;   extern __shared__ __attribute__((aligned(16))) char shm[];
;   unsigned* T = (unsigned*)(shm + FILL_LDS_OFF + bufsel * FILL_TB); const int tid = ltid(), tx = tid & 15, ty = tid >> 4;
;   constexpr float WS = (float)(1 << FP8_WSCALE_LOG2_);
; #pragma unroll
;   for (int j = 0; j < 4; ++j) T[(4 * tx + j) * 33 + ty] = cvt_pk4_fp8((f32x4){ld[0][j] * WS, ld[1][j] * WS, ld[2][j] * WS, ld[3][j] * WS});
; }
; DEV void fill_store(CParams& p, int wg, int slot, int bufsel) {
;   extern __shared__ __attribute__((aligned(16))) char shm[];
;   const unsigned* T = (const unsigned*)(shm + FILL_LDS_OFF + bufsel * FILL_TB); const int tid = ltid(), nl = tid >> 3, cc = tid & 7;
;   const FillDesc d = fill_decode(p, wg, slot);
;   u32x4 v; v.x = T[nl * 33 + 4 * cc]; v.y = T[nl * 33 + 4 * cc + 1]; v.z = T[nl * 33 + 4 * cc + 2]; v.w = T[nl * 33 + 4 * cc + 3];
;   *(u32x4*)(d.dst + (long)perm_row(d.perm, d.n0 + nl) * 2048 + d.kh + 16 * cc) = v;
; }
	v_mul_f32_e32 v11, 0x42800000, v15
	v_mov_b32_e32 v14, v19
	v_cvt_pk_fp8_f32 v14, v10, v11
	v_mul_f32_e32 v2, 0x42800000, v2
	v_mul_f32_e32 v6, 0x42800000, v6
	v_cvt_pk_fp8_f32 v21, v2, v6 op_sel:[0,0,1]
	v_mul_f32_e32 v2, 0x42800000, v3
	v_mul_f32_e32 v3, 0x42800000, v7
	v_cvt_pk_fp8_f32 v14, v2, v3 op_sel:[0,0,1]
	v_mul_f32_e32 v2, 0x42800000, v12
	v_mul_f32_e32 v3, 0x42800000, v16
	v_mov_b32_e32 v7, v19
	v_mul_f32_e32 v6, 0x42800000, v8
	v_cvt_pk_fp8_f32 v7, v2, v3
	v_mul_f32_e32 v2, 0x42800000, v13
	v_mul_f32_e32 v3, 0x42800000, v17
	v_mov_b32_e32 v8, v19
	v_mov_b32_e32 v46, v49
	v_cvt_pk_fp8_f32 v8, v2, v3
	v_pk_mul_f32 v[56:57], v[58:59], v[56:57] op_sel_hi:[0,1]
	v_pk_mul_f32 v[46:47], v[58:59], v[46:47] op_sel_hi:[0,1]
	v_mov_b32_e32 v18, v0
	v_cvt_pk_bf16_f32 v56, v56, v57
	v_cvt_pk_bf16_f32 v57, v46, v47
	ds_write_b128 v133, v[50:53]
	ds_write_b128 v134, v[54:57]
	v_mul_f32_e32 v4, 0x42800000, v4
	v_ashrrev_i32_e32 v20, 4, v18
	v_lshlrev_b32_e32 v18, 2, v18
	v_mul_f32_e32 v2, 0x42800000, v5
	v_mul_f32_e32 v3, 0x42800000, v9
	v_and_b32_e32 v18, 60, v18
	v_cvt_pk_fp8_f32 v7, v4, v6 op_sel:[0,0,1]
	v_cvt_pk_fp8_f32 v8, v2, v3 op_sel:[0,0,1]
	s_add_i32 s73, s82, 0xffffff00
	v_lshlrev_b32_e32 v20, 2, v20
	v_mul_u32_u24_e32 v2, 0x84, v18
	s_ashr_i32 s72, s73, 1
	v_add3_u32 v2, s76, v20, v2
	s_cmpk_gt_i32 s72, 0x3fff
	s_mov_b64 s[70:71], -1
	ds_write2_b32 v2, v21, v14 offset1:33
	ds_write2_b32 v2, v7, v8 offset0:66 offset1:99
	s_add_i32 s70, s82, 0xffffff00
	s_lshr_b32 s70, s70, 8
	s_lshl_b32 s70, s70, 23
	s_add_u32 s70, s64, s70
	s_addc_u32 s71, s65, 0
	s_add_u32 s70, s70, s98
	s_addc_u32 s71, s71, 0
	s_add_u32 s72, s70, 0x8000
	s_addc_u32 s73, s71, 0
	v_lshrrev_b32_e32 v2, 4, v0
	v_and_b32_e32 v3, 15, v0
	v_lshlrev_b32_e32 v2, 16, v2
	v_lshl_or_b32 v2, v3, 4, v2
	v_add_u32_e32 v3, 0x4000, v2
	v_add_u32_e32 v6, 0x4000, v2
	global_load_dwordx4 v[10:13], v2, s[70:71]
	global_load_dwordx4 v[14:17], v3, s[70:71]
	global_load_dwordx4 v[2:5], v2, s[72:73]
	s_nop 0
	global_load_dwordx4 v[6:9], v6, s[72:73]
	s_add_i32 s62, s88, 0x133f
	s_add_i32 s70, s89, 0x4c0
	s_and_b64 s[68:69], s[52:53], exec
	s_cselect_b32 s62, s70, s62
	s_sub_u32 s70, s62, 64
	s_lshl_b32 s72, s70, 11
	s_lshl_b32 s70, s70, 12
	s_add_u32 s70, s32, s70
	s_addc_u32 s71, s92, 0
	s_add_u32 s72, s93, s72
	s_addc_u32 s73, s94, 0
	s_waitcnt lgkmcnt(0)
	s_barrier
	v_add_u32_e32 v21, s76, v212
	ds_read2_b32 v[46:47], v21 offset1:1
	ds_read2_b32 v[48:49], v21 offset0:2 offset1:3
	v_lshrrev_b32_e32 v20, 1, v151
	global_load_dword v169, v20, s[72:73]
	global_load_dwordx2 v[100:101], v151, s[70:71]
	v_lshrrev_b32_e32 v21, 1, v135
	global_load_dword v168, v21, s[72:73]
	global_load_dwordx2 v[98:99], v135, s[70:71]
	v_lshrrev_b32_e32 v20, 1, v136
	global_load_dword v162, v20, s[72:73]
	global_load_dwordx2 v[96:97], v136, s[70:71]
	v_lshrrev_b32_e32 v21, 1, v137
	global_load_dword v161, v21, s[72:73]
	global_load_dwordx2 v[94:95], v137, s[70:71]
	v_lshrrev_b32_e32 v20, 1, v138
	global_load_dword v159, v20, s[72:73]
	global_load_dwordx2 v[92:93], v138, s[70:71]
	v_lshrrev_b32_e32 v21, 1, v139
	global_load_dword v158, v21, s[72:73]
	global_load_dwordx2 v[90:91], v139, s[70:71]
	v_lshrrev_b32_e32 v20, 1, v141
	global_load_dword v157, v20, s[72:73]
	global_load_dwordx2 v[88:89], v141, s[70:71]
	v_lshrrev_b32_e32 v21, 1, v143
	global_load_dword v156, v21, s[72:73]
	global_load_dwordx2 v[86:87], v143, s[70:71]
	s_sub_u32 s70, s62, 64
	s_lshl_b32 s70, s70, 11
	s_add_u32 s70, s95, s70
	s_addc_u32 s71, s96, 0
	global_load_dwordx2 v[104:105], v144, s[70:71]
	s_add_i32 s91, s82, 0xfffffd00
	s_lshr_b32 s70, s91, 8
	s_lshr_b32 s71, s70, 2
	s_lshl_b32 s71, s71, 23
	s_and_b32 s70, s70, 3
	s_lshl_b32 s70, s70, 9
	s_or_b32 s70, s70, s71
	s_add_u32 s72, s44, s70
	s_addc_u32 s73, s45, 0
	s_waitcnt lgkmcnt(0)
	global_store_dwordx4 v211, v[46:49], s[72:73]
	v_add_u32_e32 v243, v205, v206
	v_add_u32_e32 v245, v205, v208
	v_add_u32_e32 v244, v205, v207
	ds_read_b128 v[58:61], v243
	ds_read_b128 v[50:53], v244
	v_add_u32_e32 v246, v205, v209
	ds_read_b128 v[54:57], v245
	ds_read_b128 v[46:49], v246
	v_mov_b32_e32 v62, 0
	v_mov_b32_e32 v66, 0
	v_mov_b32_e32 v67, 0
	v_mov_b32_e32 v68, 0
	v_mov_b32_e32 v69, 0
	s_and_saveexec_b64 s[68:69], s[16:17]
	s_cbranch_execz .LBB0_811
	v_add_u32_e32 v18, v184, v183
	ds_read_b128 v[64:67], v18
	v_add_u32_e32 v18, v184, v182
	ds_read_b128 v[68:71], v18
	v_add_u32_e32 v18, v184, v181
	ds_read_b128 v[72:75], v18
	v_add_u32_e32 v18, v184, v180
	s_waitcnt lgkmcnt(2)
	v_mfma_f32_16x16x32_bf16 v[64:67], v[64:67], v[58:61], 0
	s_waitcnt lgkmcnt(1)
	v_mfma_f32_16x16x32_bf16 v[64:67], v[68:71], v[50:53], v[64:67]
	ds_read_b128 v[68:71], v18
	s_waitcnt lgkmcnt(1)
	v_mfma_f32_16x16x32_bf16 v[64:67], v[72:75], v[54:57], v[64:67]
	s_waitcnt lgkmcnt(0)
	v_mfma_f32_16x16x32_bf16 v[66:69], v[68:71], v[46:49], v[64:67]
	s_and_saveexec_b64 s[70:71], s[38:39]
	s_nop 6
	v_cndmask_b32_e64 v66, v66, 0, s[18:19]
	v_cndmask_b32_e64 v67, 0, v67, s[20:21]
	v_cndmask_b32_e64 v68, v68, 0, s[22:23]
	v_cndmask_b32_e64 v69, v69, 0, s[24:25]
	s_or_b64 exec, exec, s[70:71]

.LBB0_827:
	s_or_b64 exec, exec, s[68:69]
	ds_read_b128 v[62:65], v160
	ds_read_b128 v[66:69], v160 offset:64
	ds_read_b128 v[70:73], v160 offset:128
	ds_read_b128 v[74:77], v160 offset:192
	s_addk_i32 s88, 0x13bf
	s_addk_i32 s89, 0x440
	s_and_b64 s[68:69], s[52:53], exec
	s_cselect_b32 s62, s89, s88
	v_add_u32_e32 v20, s62, v186
	v_ashrrev_i32_e32 v21, 31, v20
	v_lshlrev_b64 v[20:21], 11, v[20:21]
	s_waitcnt lgkmcnt(3)
	v_mfma_f32_16x16x32_bf16 v[58:61], v[62:65], v[58:61], v[78:81]
	ds_read_b128 v[62:65], v153
	s_nop 1
	ds_read_b128 v[78:81], v153 offset:64
	ds_read_b128 v[252:255], v152
	v_cndmask_b32_e64 v18, v251, v130, s[12:13]
	v_pk_mul_f32 v[44:45], v[44:45], v[18:19] op_sel_hi:[1,0]
	s_waitcnt lgkmcnt(5)
	v_mfma_f32_16x16x32_bf16 v[50:53], v[66:69], v[50:53], v[58:61]
	v_mul_f32_e64 v42, v42, v18
	v_mul_f32_e64 v43, v43, v18
	v_pk_mul_f32 v[40:41], v[40:41], v[18:19] op_sel_hi:[1,0]
	v_pk_mul_f32 v[38:39], v[38:39], v[18:19] op_sel_hi:[1,0]
	s_waitcnt lgkmcnt(4)
	v_mfma_f32_16x16x32_bf16 v[50:53], v[70:73], v[54:57], v[50:53]
	s_waitcnt vmcnt(37)
	v_pk_mul_f32 v[60:61], v[124:125], v[126:127]
	ds_read_b128 v[54:57], v152 offset:64
	s_waitcnt vmcnt(35)
	v_pk_mul_f32 v[66:67], v[122:123], v[60:61]
	s_waitcnt lgkmcnt(4)
	v_mfma_f32_16x16x32_bf16 v[46:49], v[74:77], v[46:49], v[50:53]
	s_waitcnt vmcnt(33)
	v_pk_mul_f32 v[68:69], v[120:121], v[66:67]
	v_lshl_add_u64 v[58:59], v[110:111], 0, v[20:21]
	s_waitcnt vmcnt(31)
	v_pk_mul_f32 v[70:71], v[118:119], v[68:69]
	s_waitcnt lgkmcnt(1)
	v_mfma_f32_16x16x32_bf16 v[42:45], v[252:255], v[62:65], v[42:45]
	s_waitcnt vmcnt(29)
	v_pk_mul_f32 v[72:73], v[70:71], v[116:117]
	v_cvt_pk_bf16_f32 v50, v46, v47
	s_waitcnt vmcnt(27)
	v_pk_mul_f32 v[46:47], v[72:73], v[114:115]
	v_cvt_pk_bf16_f32 v51, v48, v49
	s_waitcnt vmcnt(25)
	v_pk_mul_f32 v[20:21], v[46:47], v[112:113]
	ds_bpermute_b32 v52, v1, v20
	ds_bpermute_b32 v53, v1, v21
	global_store_dwordx2 v[58:59], v[50:51], off
	ds_read_b128 v[48:51], v152 offset:2304
	s_waitcnt lgkmcnt(3)
	v_mfma_f32_16x16x32_bf16 v[42:45], v[54:57], v[78:81], v[42:45]
	v_add_u32_e32 v77, 0x4400, v155
	s_waitcnt lgkmcnt(1)
	v_pk_mul_f32 v[52:53], v[20:21], v[52:53]
	s_cmp_gt_u32 s57, 63
	v_cndmask_b32_e64 v57, v53, v21, s[6:7]
	v_cndmask_b32_e64 v56, v52, v20, s[6:7]
	ds_bpermute_b32 v58, v107, v56
	ds_bpermute_b32 v59, v107, v57
	s_waitcnt lgkmcnt(2)
	v_mfma_f32_16x16x32_bf16 v[38:41], v[48:51], v[62:65], v[38:41]
	ds_read_b128 v[52:55], v152 offset:2368
	s_waitcnt vmcnt(25)
	ds_write_b16 v145, v128 offset:53248
	ds_write_b16_d16_hi v145, v128 offset:53392
	ds_write_b16 v145, v129 offset:53536
	ds_write_b16_d16_hi v145, v129 offset:53680
	s_waitcnt lgkmcnt(5)
	v_pk_mul_f32 v[48:49], v[56:57], v[58:59]
	s_waitcnt lgkmcnt(4)
	v_mfma_f32_16x16x32_bf16 v[38:41], v[52:55], v[78:81], v[38:41]
	v_cndmask_b32_e64 v49, v49, v57, s[8:9]
	v_cndmask_b32_e64 v48, v48, v56, s[8:9]
	ds_bpermute_b32 v50, v131, v48
	ds_bpermute_b32 v51, v131, v49
	v_add_u32_e32 v53, v185, v192
	v_add_u32_e32 v55, v185, v193
	s_cselect_b64 s[68:69], -1, 0
	s_and_b64 vcc, exec, s[68:69]
	s_waitcnt lgkmcnt(0)
	v_pk_mul_f32 v[50:51], v[48:49], v[50:51]
	s_nop 0
	v_cndmask_b32_e64 v18, v50, v48, s[10:11]
	ds_bpermute_b32 v48, v1, v18
	v_cndmask_b32_e64 v49, v51, v49, s[10:11]
	ds_bpermute_b32 v51, v150, v18
	ds_bpermute_b32 v50, v1, v49
	ds_bpermute_b32 v54, v148, v49
	s_waitcnt lgkmcnt(3)
	v_cndmask_b32_e64 v59, 1.0, v48, s[4:5]
	ds_bpermute_b32 v48, v148, v18
	ds_bpermute_b32 v18, v150, v49
	s_waitcnt lgkmcnt(4)
	v_max_f32_e32 v49, v51, v51
	v_max_f32_e32 v49, 0x554ad2e, v49
	v_rcp_f32_e32 v74, v49
	ds_bpermute_b32 v49, v132, v51
	s_waitcnt lgkmcnt(1)
	ds_bpermute_b32 v51, v132, v18
	v_max_f32_e32 v18, v18, v18
	v_max_f32_e32 v52, 0x554ad2e, v18
	v_rcp_f32_e32 v76, v52
	v_cndmask_b32_e64 v75, 1.0, v50, s[4:5]
	s_waitcnt lgkmcnt(0)
	v_cndmask_b32_e64 v49, v51, v49, s[12:13]
	v_mul_f32_e32 v51, v42, v49
	v_cvt_pk_bf16_f32 v51, v51, s0
	ds_write_b16 v53, v51 offset:57856
	v_mul_f32_e32 v51, v43, v49
	v_cvt_pk_bf16_f32 v51, v51, s0
	ds_write_b16 v53, v51 offset:58128
	v_mul_f32_e32 v51, v44, v49
	v_cvt_pk_bf16_f32 v51, v51, s0
	ds_write_b16 v55, v51 offset:57856
	v_mul_f32_e32 v51, v45, v49
	v_cvt_pk_bf16_f32 v51, v51, s0
	ds_write_b16 v55, v51 offset:58128
	v_mul_f32_e32 v51, v38, v49
	v_cvt_pk_bf16_f32 v51, v51, s0
	ds_write_b16 v53, v51 offset:62208
	v_mul_f32_e32 v51, v39, v49
	v_cvt_pk_bf16_f32 v51, v51, s0
	ds_write_b16 v53, v51 offset:62480
	v_mul_f32_e32 v51, v40, v49
	v_mul_f32_e32 v49, v41, v49
	v_cvt_pk_bf16_f32 v49, v49, s0
	ds_write_b16 v53, v49 offset:63024
	v_mul_f32_e32 v49, v126, v59
	v_mul_f32_e32 v49, v49, v74
	v_med3_f32 v50, v49, s85, v213
	v_mul_f32_e32 v49, v127, v75
	v_cvt_pk_bf16_f32 v51, v51, s0
	v_mul_f32_e32 v49, v49, v76
	ds_write_b16 v53, v51 offset:62752
	v_med3_f32 v51, v49, s85, v213
	v_rcp_f32_e32 v52, v50
	v_rcp_f32_e32 v53, v51
	v_mul_f32_e32 v56, v60, v59
	v_mul_f32_e32 v57, v61, v75
	v_mul_f32_e32 v56, v56, v74
	v_mul_f32_e32 v57, v57, v76
	v_med3_f32 v56, v56, s85, v213
	v_med3_f32 v57, v57, s85, v213
	v_mul_f32_e32 v58, v76, v54
	ds_bpermute_b32 v49, v132, v54
	v_pk_add_f32 v[54:55], v[126:127], 1.0 op_sel_hi:[1,0] neg_lo:[1,0] neg_hi:[1,0]
	v_rcp_f32_e32 v60, v56
	v_rcp_f32_e32 v61, v57
	v_pk_mul_f32 v[52:53], v[54:55], v[52:53]
	v_lshlrev_b32_e32 v54, 16, v250
	v_and_b32_e32 v55, 0xffff0000, v250
	v_pk_mul_f32 v[50:51], v[50:51], v[54:55]
	v_cvt_pk_bf16_f32 v62, v52, v53
	v_cvt_pk_bf16_f32 v63, v50, v51
	v_pk_add_f32 v[50:51], v[124:125], 1.0 op_sel_hi:[1,0] neg_lo:[1,0] neg_hi:[1,0]
	v_and_b32_e32 v55, 0xffff0000, v249
	v_pk_mul_f32 v[50:51], v[50:51], v[60:61]
; DEV int ltid() { int t = threadIdx.x; asm volatile("" : "+v"(t)); return t; }
; DEV unsigned cvt_pk4_fp8(f32x4 v) { unsigned r = 0; r = __builtin_amdgcn_cvt_pk_fp8_f32(v[0], v[1], r, false); r = __builtin_amdgcn_cvt_pk_fp8_f32(v[2], v[3], r, true); return r; }
; DEV void fill_load(CParams& p, int wg, int slot, f32x4 (&ld)[4]) {
;   const FillDesc d = fill_decode(p, wg, slot); const int tid = ltid(), tx = tid & 15, ty = tid >> 4;
;   const float* sp = d.src + (long)(d.kh + 4 * ty) * d.ldsrc + d.n0 + 4 * tx;
; #pragma unroll
;   for (int r = 0; r < 4; ++r) ld[r] = *(const f32x4*)(sp + (long)r * d.ldsrc);
; }
; DEV void fill_write(const f32x4 (&ld)[4], int bufsel) {
;   extern __shared__ __attribute__((aligned(16))) char shm[];
;   unsigned* T = (unsigned*)(shm + FILL_LDS_OFF + bufsel * FILL_TB); const int tid = ltid(), tx = tid & 15, ty = tid >> 4;
;   constexpr float WS = (float)(1 << FP8_WSCALE_LOG2_);
; #pragma unroll
;   for (int j = 0; j < 4; ++j) T[(4 * tx + j) * 33 + ty] = cvt_pk4_fp8((f32x4){ld[0][j] * WS, ld[1][j] * WS, ld[2][j] * WS, ld[3][j] * WS});
; }
	v_mul_f32_e32 v18, v74, v48
	v_cvt_pk_bf16_f32 v54, v50, v51
	ds_write2_b32 v77, v62, v54 offset1:68
	v_lshlrev_b32_e32 v54, 16, v249
	v_pk_mul_f32 v[54:55], v[56:57], v[54:55]
	v_mul_f32_e32 v46, v46, v59
	v_cvt_pk_bf16_f32 v54, v54, v55
	v_mov_b32_e32 v55, v50
	v_mov_b32_e32 v50, v53
	ds_write2_b32 v155, v63, v54 offset1:68
	v_mov_b32_e32 v54, v52
	v_pk_mul_f32 v[52:53], v[58:59], v[50:51] op_sel_hi:[0,1]
	v_mul_f32_e32 v50, v66, v59
	v_mul_f32_e32 v50, v50, v74
	v_med3_f32 v56, v50, s85, v213
	v_mul_f32_e32 v50, v67, v75
	v_pk_mul_f32 v[54:55], v[18:19], v[54:55] op_sel_hi:[0,1]
	v_mul_f32_e32 v50, v50, v76
	v_med3_f32 v57, v50, s85, v213
	v_cvt_pk_bf16_f32 v50, v54, v55
	v_mul_f32_e32 v55, v68, v59
	v_mul_f32_e32 v55, v55, v74
	v_rcp_f32_e32 v60, v56
	v_rcp_f32_e32 v61, v57
	v_med3_f32 v62, v55, s85, v213
	v_mul_f32_e32 v55, v69, v75
	v_mul_f32_e32 v55, v55, v76
	v_med3_f32 v63, v55, s85, v213
	v_cvt_pk_bf16_f32 v54, v52, v53
	v_pk_add_f32 v[52:53], v[122:123], 1.0 op_sel_hi:[1,0] neg_lo:[1,0] neg_hi:[1,0]
	v_rcp_f32_e32 v64, v62
	v_rcp_f32_e32 v65, v63
	v_pk_mul_f32 v[52:53], v[52:53], v[60:61]
	v_lshlrev_b32_e32 v60, 16, v248
	v_and_b32_e32 v61, 0xffff0000, v248
	v_pk_mul_f32 v[56:57], v[56:57], v[60:61]
	v_cvt_pk_bf16_f32 v51, v52, v53
	v_cvt_pk_bf16_f32 v55, v56, v57
	v_pk_add_f32 v[56:57], v[120:121], 1.0 op_sel_hi:[1,0] neg_lo:[1,0] neg_hi:[1,0]
	v_and_b32_e32 v61, 0xffff0000, v247
	v_pk_mul_f32 v[56:57], v[56:57], v[64:65]
	v_add_u32_e32 v68, 0x4800, v155
	v_cvt_pk_bf16_f32 v60, v56, v57
	ds_write2_b32 v77, v51, v60 offset0:136 offset1:204
	v_lshlrev_b32_e32 v60, 16, v247
	v_pk_mul_f32 v[60:61], v[62:63], v[60:61]
	v_mul_f32_e32 v47, v47, v75
	v_cvt_pk_bf16_f32 v51, v60, v61
	ds_write2_b32 v155, v55, v51 offset0:136 offset1:204
	v_mul_f32_e32 v51, v70, v59
	v_mov_b32_e32 v61, v56
	v_mov_b32_e32 v56, v53
	v_mul_f32_e32 v51, v51, v74
	v_mov_b32_e32 v60, v52
	v_pk_mul_f32 v[52:53], v[58:59], v[56:57] op_sel_hi:[0,1]
	v_med3_f32 v56, v51, s85, v213
	v_mul_f32_e32 v51, v71, v75
	v_mul_f32_e32 v51, v51, v76
	v_med3_f32 v57, v51, s85, v213
	v_rcp_f32_e32 v62, v56
	v_rcp_f32_e32 v63, v57
	v_cvt_pk_bf16_f32 v55, v52, v53
	v_pk_add_f32 v[52:53], v[118:119], 1.0 op_sel_hi:[1,0] neg_lo:[1,0] neg_hi:[1,0]
	v_pk_mul_f32 v[60:61], v[18:19], v[60:61] op_sel_hi:[0,1]
	v_pk_mul_f32 v[52:53], v[52:53], v[62:63]
	v_mul_f32_e32 v62, v72, v59
	v_mul_f32_e32 v63, v73, v75
	v_mul_f32_e32 v62, v62, v74
	v_mul_f32_e32 v63, v63, v76
	v_med3_f32 v62, v62, s85, v213
	v_med3_f32 v63, v63, s85, v213
	v_rcp_f32_e32 v64, v62
	v_rcp_f32_e32 v65, v63
	v_cvt_pk_bf16_f32 v51, v60, v61
	v_lshlrev_b32_e32 v60, 16, v242
	v_and_b32_e32 v61, 0xffff0000, v242
	v_pk_mul_f32 v[56:57], v[56:57], v[60:61]
	v_cvt_pk_bf16_f32 v66, v52, v53
	v_cvt_pk_bf16_f32 v67, v56, v57
	v_pk_add_f32 v[56:57], v[116:117], 1.0 op_sel_hi:[1,0] neg_lo:[1,0] neg_hi:[1,0]
	v_and_b32_e32 v61, 0xffff0000, v240
	v_pk_mul_f32 v[56:57], v[56:57], v[64:65]
	v_mul_f32_e32 v46, v46, v74
	v_cvt_pk_bf16_f32 v60, v56, v57
	ds_write2_b32 v68, v66, v60 offset0:16 offset1:84
	v_lshlrev_b32_e32 v60, 16, v240
	v_mul_f32_e32 v47, v47, v76
	v_pk_mul_f32 v[60:61], v[62:63], v[60:61]
	v_med3_f32 v46, v46, s85, v213
	v_med3_f32 v47, v47, s85, v213
	v_cvt_pk_bf16_f32 v60, v60, v61
	v_add_u32_e32 v66, 0x400, v155
	v_rcp_f32_e32 v62, v46
	v_rcp_f32_e32 v63, v47
	v_mul_f32_e32 v20, v20, v59
	v_mul_f32_e32 v21, v21, v75
	ds_write2_b32 v66, v67, v60 offset0:16 offset1:84
	v_mov_b32_e32 v60, v52
	v_mov_b32_e32 v61, v56
	v_mul_f32_e32 v20, v20, v74
	v_mul_f32_e32 v21, v21, v76
	v_pk_mul_f32 v[60:61], v[18:19], v[60:61] op_sel_hi:[0,1]
	v_med3_f32 v20, v20, s85, v213
	v_med3_f32 v21, v21, s85, v213
	v_cvt_pk_bf16_f32 v52, v60, v61
	v_pk_add_f32 v[60:61], v[114:115], 1.0 op_sel_hi:[1,0] neg_lo:[1,0] neg_hi:[1,0]
	v_rcp_f32_e32 v64, v20
	v_rcp_f32_e32 v65, v21
	v_mov_b32_e32 v56, v53
	v_pk_mul_f32 v[60:61], v[60:61], v[62:63]
	v_lshlrev_b32_e32 v62, 16, v239
	v_and_b32_e32 v63, 0xffff0000, v239
	v_pk_mul_f32 v[56:57], v[58:59], v[56:57] op_sel_hi:[0,1]
	v_pk_mul_f32 v[46:47], v[46:47], v[62:63]
	v_lshlrev_b32_e32 v62, 16, v238
	v_and_b32_e32 v63, 0xffff0000, v238
	v_cvt_pk_bf16_f32 v56, v56, v57
	v_cvt_pk_bf16_f32 v57, v46, v47
	v_pk_add_f32 v[46:47], v[112:113], 1.0 op_sel_hi:[1,0] neg_lo:[1,0] neg_hi:[1,0]
	v_pk_mul_f32 v[20:21], v[20:21], v[62:63]
	v_pk_mul_f32 v[46:47], v[46:47], v[64:65]
	v_cvt_pk_bf16_f32 v20, v20, v21
	ds_write2_b32 v66, v57, v20 offset0:152 offset1:220
	v_mov_b32_e32 v20, v60
	v_mov_b32_e32 v21, v46
	v_cvt_pk_bf16_f32 v53, v60, v61
	v_cvt_pk_bf16_f32 v59, v46, v47
	v_pk_mul_f32 v[20:21], v[18:19], v[20:21] op_sel_hi:[0,1]
	v_mov_b32_e32 v46, v61
	ds_write2_b32 v68, v53, v59 offset0:152 offset1:220
	v_pk_mul_f32 v[46:47], v[58:59], v[46:47] op_sel_hi:[0,1]
	v_cvt_pk_bf16_f32 v53, v20, v21
	v_cvt_pk_bf16_f32 v57, v46, v47
	ds_write_b128 v146, v[50:53] offset:34816
	ds_write_b128 v147, v[54:57] offset:34816
	v_mul_f32_e32 v21, 0x42800000, v22
	v_mul_f32_e32 v46, 0x42800000, v26
	v_mov_b32_e32 v51, v19
	v_cvt_pk_fp8_f32 v51, v21, v46
	v_mul_f32_e32 v21, 0x42800000, v23
	v_mul_f32_e32 v46, 0x42800000, v27
	v_mov_b32_e32 v52, v19
	v_cvt_pk_fp8_f32 v52, v21, v46
	v_mul_f32_e32 v21, 0x42800000, v31
	v_mul_f32_e32 v46, 0x42800000, v35
	v_mov_b32_e32 v53, v19
	v_cvt_pk_fp8_f32 v52, v21, v46 op_sel:[0,0,1]
	v_mul_f32_e32 v21, 0x42800000, v24
	v_mul_f32_e32 v46, 0x42800000, v28
	v_cvt_pk_fp8_f32 v53, v21, v46
	v_mul_f32_e32 v21, 0x42800000, v25
	v_mul_f32_e32 v46, 0x42800000, v29
	v_mov_b32_e32 v54, v19
	v_cvt_pk_fp8_f32 v54, v21, v46
	v_mov_b32_e32 v18, v0
	ds_bpermute_b32 v48, v132, v48
	v_mul_f32_e32 v47, 0x42800000, v30
	v_mul_f32_e32 v50, 0x42800000, v34
	v_ashrrev_i32_e32 v20, 4, v18
	v_lshlrev_b32_e32 v18, 2, v18
	v_cvt_pk_fp8_f32 v51, v47, v50 op_sel:[0,0,1]
	v_mul_f32_e32 v47, 0x42800000, v32
	v_mul_f32_e32 v50, 0x42800000, v36
	v_mul_f32_e32 v21, 0x42800000, v33
	v_mul_f32_e32 v46, 0x42800000, v37
	v_and_b32_e32 v18, 60, v18
	v_cvt_pk_fp8_f32 v53, v47, v50 op_sel:[0,0,1]
	v_cvt_pk_fp8_f32 v54, v21, v46 op_sel:[0,0,1]
	v_lshlrev_b32_e32 v20, 2, v20
	v_mul_u32_u24_e32 v18, 0x84, v18
	v_add3_u32 v18, s81, v20, v18
	ds_write2_b32 v18, v51, v52 offset1:33
	ds_write2_b32 v18, v53, v54 offset0:66 offset1:99
	s_cbranch_vccnz .LBB0_769
	s_lshr_b32 s70, s82, 8
	s_lshl_b32 s70, s70, 23
	s_add_u32 s70, s64, s70
	s_addc_u32 s71, s65, 0
	s_add_u32 s70, s70, s98
	s_addc_u32 s71, s71, 0
	s_add_u32 s72, s70, 0x8000
	s_addc_u32 s73, s71, 0
	v_lshrrev_b32_e32 v20, 4, v0
	v_and_b32_e32 v21, 15, v0
	v_lshlrev_b32_e32 v20, 16, v20
	v_lshl_or_b32 v20, v21, 4, v20
	v_add_u32_e32 v21, 0x4000, v20
	global_load_dwordx4 v[22:25], v20, s[70:71]
	global_load_dwordx4 v[26:29], v21, s[70:71]
	global_load_dwordx4 v[30:33], v20, s[72:73]
	s_nop 0
	global_load_dwordx4 v[34:37], v21, s[72:73]
	s_branch .LBB0_769

; DEV int ltid() { int t = threadIdx.x; asm volatile("" : "+v"(t)); return t; }
; DEV FillDesc fill_decode(CParams& p, int wg, int slot) {
;   const int h = slot * 256 + wg, t = h >> 1, half = h & 1; FillDesc d;
;   if (t < NE * 512) { const int e = t >> 9, r = t & 511; d.src = p.w_gu + (long)e * 2048 * 4096; d.ldsrc = 4096; d.dst = p.wt_gu8 + (long)e * 4096 * 2048; d.perm = 2; d.n0 = (r & 31) * 128 + 64 * half; d.kh = (r >> 5) * 128; }
;   else { const int v = t - NE * 512, e = v >> 8, r = v & 255; d.src = p.w_dn + (long)e * 2048 * 2048; d.ldsrc = 2048; d.dst = p.wt_dn8 + (long)e * 2048 * 2048; d.perm = 0; d.n0 = (r & 15) * 128 + 64 * half; d.kh = (r >> 4) * 128; }
;   return d;
; }
; DEV void fill_load(CParams& p, int wg, int slot, f32x4 (&ld)[4]) {
;   const FillDesc d = fill_decode(p, wg, slot); const int tid = ltid(), tx = tid & 15, ty = tid >> 4;
;   const float* sp = d.src + (long)(d.kh + 4 * ty) * d.ldsrc + d.n0 + 4 * tx;
; #pragma unroll
;   for (int r = 0; r < 4; ++r) ld[r] = *(const f32x4*)(sp + (long)r * d.ldsrc);
; }
; DEV void hgrn_unit(CParams& p, int u, int wg, bool fill) {
;     ...
;   f32x4 fldA[4], fldB[4];
;   if (fill && FILL_HG > 0) { fill_load(p, wg, 0, fldA); if (FILL_HG > 1) fill_load(p, wg, 1, fldB); }
;   HG_LOAD(0, g, q, v);
;   HG_ELEM(0, false);
;   HG_LOAD(1, g, q, v);
;   __syncthreads();
;   HG_STEP(0, false, false, fldA); HG_STEP(1, false, false, fldB); HG_STEP(2, false, false, fldA);
.LBB0_971:
	v_or_b32_e32 v18, v108, v109
	v_mov_b32_e32 v22, v0
	v_add_u32_e32 v195, v18, v116
	v_add_u32_e32 v196, v18, v111
	s_lshl_b32 s21, s25, s21
	s_lshl_b32 s22, s25, 7
	v_ashrrev_i32_e32 v18, 2, v22
	s_and_b32 s21, s21, 0x780
	v_and_b32_e32 v18, -4, v18
	s_and_b32 s22, s24, s22
	v_add_u32_e32 v18, s21, v18
	s_or_b32 s24, s22, s53
	v_mad_i64_i32 v[18:19], s[22:23], s20, v18, 0
	v_lshl_add_u64 v[18:19], v[18:19], 2, s[18:19]
	s_lshl_b32 s62, s24, 2
	s_mov_b32 s63, 0
	v_lshl_add_u64 v[20:21], v[18:19], 0, s[62:63]
	v_lshlrev_b32_e32 v18, 4, v22
	v_and_b32_e32 v18, 0xf0, v18
	v_mov_b32_e32 v19, 0
	v_lshl_add_u64 v[20:21], v[20:21], 0, v[18:19]
	s_lshl_b32 s62, s20, 2
	v_lshl_add_u64 v[30:31], v[20:21], 0, s[62:63]
	global_load_dwordx4 v[22:25], v[20:21], off
	global_load_dwordx4 v[26:29], v[30:31], off
	v_lshl_add_u64 v[20:21], v[30:31], 0, s[62:63]
	s_waitcnt lgkmcnt(12)
	v_cndmask_b32_e64 v130, v36, v35, s[12:13]
	v_lshl_add_u64 v[48:49], v[20:21], 0, s[62:63]
	global_load_dwordx4 v[30:33], v[20:21], off
	global_load_dwordx4 v[34:37], v[48:49], off
	s_add_u32 s16, s16, s56
	s_addc_u32 s17, s17, 0
	s_add_u32 s16, s16, s60
	s_addc_u32 s17, s17, 0
	v_mov_b32_e32 v59, v19
	v_lshl_add_u64 v[108:109], s[16:17], 0, v[58:59]
	s_add_u32 s16, s58, s56
	s_addc_u32 s17, s59, 0
	v_ashrrev_i32_e32 v48, 7, v112
	s_add_u32 s16, s16, s60
	v_lshl_or_b32 v18, v48, 4, v113
	s_movk_i32 s62, 0x110
	v_and_b32_e32 v106, 16, v110
	s_addc_u32 s17, s17, 0
	v_mul_lo_u32 v49, v18, s62
	v_lshlrev_b32_e32 v52, 1, v18
	v_mul_lo_u32 v107, v18, s36
	v_lshlrev_b32_e32 v18, 1, v106
	v_or_b32_e32 v47, 3, v254
	v_lshl_add_u64 v[20:21], s[16:17], 0, v[18:19]
	v_lshlrev_b32_e32 v18, 1, v254
	s_add_i32 s16, 0, 0x1e600
	s_add_i32 s61, 0, 0x10400
	s_waitcnt lgkmcnt(0)
	s_barrier
	s_load_dwordx4 s[44:47], s[14:15], 0xe8
	v_add_u32_e32 v203, 0, v49
	v_lshl_add_u64 v[110:111], v[20:21], 0, v[18:19]
	v_add3_u32 v205, s16, v51, v46
	s_load_dwordx2 s[64:65], s[14:15], 0xa0
	s_load_dwordx2 s[66:67], s[14:15], 0xb0
	v_add_u32_e32 v206, s61, v49
	v_or_b32_e32 v21, 64, v115
	v_or_b32_e32 v49, 0x80, v115
	v_or_b32_e32 v51, 0xc0, v115
	v_cmp_gt_u32_e64 s[24:25], v47, v113
	v_or_b32_e32 v47, 32, v46
	s_movk_i32 s26, 0x70
	v_bitop3_b32 v184, v46, v115, 16 bitop3:0x6c
	v_bitop3_b32 v183, v46, v21, 16 bitop3:0x6c
	v_bitop3_b32 v182, v46, v49, 16 bitop3:0x6c
	v_bitop3_b32 v181, v46, v51, 16 bitop3:0x6c
	v_bitop3_b32 v179, v47, v115, 48 bitop3:0x6c
	v_bitop3_b32 v178, v47, v21, 48 bitop3:0x6c
	v_bitop3_b32 v177, v47, v49, 48 bitop3:0x6c
	v_bitop3_b32 v176, v47, v51, 48 bitop3:0x6c
	v_or_b32_e32 v47, 64, v46
	s_movk_i32 s27, 0x50
	v_or_b32_e32 v46, 0x60, v46
	v_or_b32_e32 v53, v106, v113
	v_bitop3_b32 v208, v52, v21, s26 bitop3:0x6c
	v_bitop3_b32 v173, v47, v21, s27 bitop3:0x6c
	v_bitop3_b32 v166, v46, v21, s26 bitop3:0x6c
	v_mov_b32_e32 v21, s81
	v_mul_u32_u24_e32 v204, 0x110, v53
	v_mul_u32_u24_e32 v18, 0x48, v53
	v_add_u32_e32 v20, s16, v115
	s_movk_i32 s14, 0x80
	v_mad_u32_u24 v192, v113, s62, 0
	v_mad_u32_u24 v185, v113, s62, v21
	v_mul_u32_u24_e32 v193, 0x440, v70
	v_mul_u32_u24_e32 v194, 0x110, v50
	v_add_u32_e32 v197, 0x220, v195
	v_add_u32_e32 v198, 0x330, v195
	v_add_u32_e32 v199, 0x440, v195
	v_add_u32_e32 v200, 0x550, v195
	v_add_u32_e32 v201, 0x660, v195
	v_add_u32_e32 v202, 0x770, v195
	s_mov_b32 s57, 4
	v_mul_u32_u24_e32 v188, 0x90, v53
	v_lshl_add_u32 v189, v70, 3, 0
	v_add_u32_e32 v187, 0xfffffc00, v107
	v_bitop3_b32 v207, v52, v115, s26 bitop3:0x6c
	v_bitop3_b32 v209, v52, v49, s26 bitop3:0x6c
	v_bitop3_b32 v210, v52, v51, s26 bitop3:0x6c
	v_cmp_lt_i32_e64 s[16:17], -1, v48
	v_cmp_gt_u32_e64 s[38:39], s14, v112
	v_cmp_gt_u32_e64 s[18:19], v254, v113
	v_cmp_lt_u32_e64 s[20:21], v254, v113
	v_cmp_gt_u32_e64 s[22:23], v50, v113
	v_cmp_lt_i32_e64 s[36:37], 0, v48
	v_add_u32_e32 v191, 0x1100, v192
	v_cmp_eq_u32_e64 s[34:35], 1, v48
	v_cmp_lt_i32_e64 s[14:15], 1, v48
	v_add_u32_e32 v190, 0x2200, v192
	v_bitop3_b32 v174, v47, v115, s27 bitop3:0x6c
	v_bitop3_b32 v172, v47, v49, s27 bitop3:0x6c
	v_bitop3_b32 v171, v47, v51, s27 bitop3:0x6c
	v_cmp_eq_u32_e64 s[30:31], 2, v48
	v_cmp_lt_i32_e64 s[28:29], 2, v48
	v_bitop3_b32 v169, v46, v115, s26 bitop3:0x6c
	v_bitop3_b32 v165, v46, v49, s26 bitop3:0x6c
	v_bitop3_b32 v164, v46, v51, s26 bitop3:0x6c
	v_cmp_eq_u32_e64 s[26:27], 3, v48
	v_add_u32_e32 v180, 0x1100, v185
	v_add_u32_e32 v175, 0x2200, v185
	v_add_u32_e32 v168, 0x3300, v185
	v_add_lshl_u32 v211, v18, v254, 1
	s_add_i32 s83, s2, 0x700
	s_movk_i32 s84, 0x84
	s_movk_i32 s85, 0x7ff
	s_mov_b32 s86, 0xda24260
	v_mov_b32_e32 v212, 0xfffff800
	v_mov_b32_e32 v213, 0x80
	v_mov_b32_e32 v214, 0x7149f2ca
	v_add_u32_e32 v162, v20, v204
	s_mov_b32 s87, 0
	s_mov_b32 s88, 0
	v_readfirstlane_b32 s32, v84
	v_readfirstlane_b32 s93, v85
	v_readfirstlane_b32 s94, v86
	v_readfirstlane_b32 s95, v87
	v_readfirstlane_b32 s96, v108
	v_readfirstlane_b32 s97, v109
	s_nop 1
	v_subrev_u32_e32 v84, s32, v84
	v_add_u32_e32 v84, 0x40000, v84
	v_subrev_u32_e32 v108, s96, v108
	v_add_u32_e32 v108, 0x20000, v108
	v_lshl_add_u32 v152, v152, 12, v84
	v_lshl_add_u32 v136, v136, 12, v84
	v_lshl_add_u32 v137, v137, 12, v84
	v_lshl_add_u32 v138, v138, 12, v84
	v_lshl_add_u32 v139, v139, 12, v84
	v_lshl_add_u32 v140, v140, 12, v84
	v_lshl_add_u32 v142, v142, 12, v84
	v_lshl_add_u32 v144, v144, 12, v84
	v_lshl_add_u32 v145, v145, 11, v108
	s_waitcnt lgkmcnt(0)
	s_lshr_b32 s70, s2, 1
	s_and_b32 s71, s70, 31
	s_lshl_b32 s71, s71, 7
	s_or_b32 s71, s71, s53
	s_lshr_b32 s72, s70, 5
	s_lshl_b32 s72, s72, 7
	v_lshrrev_b32_e32 v20, 3, v0
	v_and_b32_e32 v21, 7, v0
	v_lshlrev_b32_e32 v21, 4, v21
	v_mul_u32_u24_e32 v213, 0x84, v20
	v_add_u32_e32 v213, v213, v21
	v_add_u32_e32 v212, s71, v20
	v_and_b32_e32 v46, 0x7ff, v212
	v_lshrrev_b32_e32 v212, 11, v212
	v_lshlrev_b32_e32 v212, 7, v212
	v_and_b32_e32 v47, 0x7f, v46
	v_or_b32_e32 v212, v212, v47
	v_lshrrev_b32_e32 v46, 7, v46
	v_lshl_or_b32 v212, v46, 8, v212
	v_lshlrev_b32_e32 v212, 11, v212
	v_add_u32_e32 v212, v212, v21
	v_add_u32_e32 v212, s72, v212
	s_lshl_b32 s98, s72, 14
	s_lshl_b32 s73, s71, 2
	s_add_u32 s98, s98, s73
	s_branch .LBB0_975

.LBB0_1002:
	s_or_b64 exec, exec, s[68:69]
	v_add_u32_e32 v218, v149, v204
	ds_read_b128 v[62:65], v218 offset:57856
	ds_read_b128 v[66:69], v218 offset:57920
	ds_read_b128 v[70:73], v143 offset:34816
	ds_read_b128 v[74:77], v143 offset:34880
	ds_read_b128 v[224:227], v218 offset:57984
	s_add_i32 s62, s89, 0x13ff
	s_add_i32 s70, s90, 0x400
	v_pk_mul_f32 v[44:45], v[44:45], v[130:131] op_sel_hi:[1,0]
	v_pk_mul_f32 v[42:43], v[42:43], v[130:131] op_sel_hi:[1,0]
	s_and_b64 s[68:69], s[54:55], exec
	s_cselect_b32 s62, s70, s62
	s_waitcnt lgkmcnt(4)
	v_mfma_f32_16x16x32_bf16 v[58:61], v[62:65], v[58:61], v[78:81]
	ds_read_b128 v[62:65], v155 offset:53248
	s_nop 1
	ds_read_b128 v[78:81], v218 offset:58048
	v_add_u32_e32 v20, s62, v187
	v_ashrrev_i32_e32 v21, 31, v20
	s_waitcnt lgkmcnt(5)
	v_mfma_f32_16x16x32_bf16 v[50:53], v[66:69], v[50:53], v[58:61]
	v_lshlrev_b64 v[20:21], 11, v[20:21]
	v_pk_mul_f32 v[40:41], v[40:41], v[130:131] op_sel_hi:[1,0]
	v_pk_mul_f32 v[38:39], v[38:39], v[130:131] op_sel_hi:[1,0]
	s_waitcnt lgkmcnt(2)
	v_mfma_f32_16x16x32_bf16 v[50:53], v[224:227], v[54:57], v[50:53]
	s_waitcnt vmcnt(33)
	v_pk_mul_f32 v[60:61], v[100:101], v[102:103]
	ds_read_b128 v[54:57], v155 offset:53312
	v_lshl_add_u64 v[58:59], v[110:111], 0, v[20:21]
	s_waitcnt lgkmcnt(1)
	v_mfma_f32_16x16x32_bf16 v[48:51], v[78:81], v[46:49], v[50:53]
	v_add_u32_e32 v215, v205, v193
	v_add_u32_e32 v219, v205, v194
	v_add_u32_e32 v222, s81, v195
	v_mfma_f32_16x16x32_bf16 v[42:45], v[62:65], v[70:73], v[42:45]
	s_waitcnt vmcnt(31)
	v_pk_mul_f32 v[62:63], v[98:99], v[60:61]
	s_nop 1
	v_cvt_pk_bf16_f32 v52, v48, v49
	s_waitcnt vmcnt(29)
	v_pk_mul_f32 v[64:65], v[96:97], v[62:63]
	v_cvt_pk_bf16_f32 v53, v50, v51
	s_waitcnt vmcnt(27)
	v_pk_mul_f32 v[66:67], v[94:95], v[64:65]
	global_store_dwordx2 v[58:59], v[52:53], off offset:1024
	s_waitcnt vmcnt(26)
	v_pk_mul_f32 v[48:49], v[92:93], v[66:67]
	ds_read_b128 v[50:53], v155 offset:55552
	s_waitcnt vmcnt(24)
	v_pk_mul_f32 v[46:47], v[90:91], v[48:49]
	s_waitcnt lgkmcnt(1)
	v_mfma_f32_16x16x32_bf16 v[42:45], v[54:57], v[74:77], v[42:45]
	s_waitcnt vmcnt(22)
	v_pk_mul_f32 v[20:21], v[88:89], v[46:47]
	ds_bpermute_b32 v68, v1, v20
	ds_bpermute_b32 v69, v1, v21
	s_waitcnt lgkmcnt(2)
	v_mfma_f32_16x16x32_bf16 v[38:41], v[50:53], v[70:73], v[38:41]
	s_waitcnt lgkmcnt(0)
	v_pk_mul_f32 v[54:55], v[20:21], v[68:69]
	v_add_u32_e32 v224, s61, v195
	v_cndmask_b32_e64 v59, v55, v21, s[6:7]
	v_cndmask_b32_e64 v58, v54, v20, s[6:7]
	ds_bpermute_b32 v68, v131, v58
	ds_bpermute_b32 v69, v131, v59
	ds_read_b128 v[54:57], v155 offset:55616
	s_waitcnt lgkmcnt(0)
	v_mfma_f32_16x16x32_bf16 v[38:41], v[54:57], v[74:77], v[38:41]
	v_mul_f32_e64 v50, v58, v68
	v_mul_f32_e64 v51, v59, v69
	s_waitcnt vmcnt(21)
	ds_write_b16 v141, v104
	ds_write_b16_d16_hi v141, v104 offset:144
	ds_write_b16 v141, v105 offset:288
	v_cndmask_b32_e64 v51, v51, v59, s[8:9]
	v_cndmask_b32_e64 v50, v50, v58, s[8:9]
	ds_bpermute_b32 v52, v132, v50
	ds_bpermute_b32 v53, v132, v51
	ds_write_b16_d16_hi v141, v105 offset:432
	v_add_u32_e32 v225, s81, v196
	v_add_u32_e32 v226, s61, v196
	v_add_u32_e32 v227, s81, v197
	s_waitcnt lgkmcnt(1)
	v_pk_mul_f32 v[52:53], v[50:51], v[52:53]
	v_add_u32_e32 v228, s61, v197
	v_cndmask_b32_e64 v18, v52, v50, s[10:11]
	ds_bpermute_b32 v50, v1, v18
	v_cndmask_b32_e64 v51, v53, v51, s[10:11]
	ds_bpermute_b32 v53, v151, v18
	ds_bpermute_b32 v52, v1, v51
	ds_bpermute_b32 v54, v150, v51
	s_waitcnt lgkmcnt(3)
	v_cndmask_b32_e64 v59, 1.0, v50, s[4:5]
	ds_bpermute_b32 v50, v150, v18
	ds_bpermute_b32 v18, v151, v51
	s_waitcnt lgkmcnt(4)
	v_max_f32_e32 v51, v53, v53
	v_max_f32_e32 v51, 0x554ad2e, v51
	v_rcp_f32_e32 v68, v51
	ds_bpermute_b32 v51, v133, v53
	s_waitcnt lgkmcnt(1)
	ds_bpermute_b32 v53, v133, v18
	v_max_f32_e32 v18, v18, v18
	v_max_f32_e32 v55, 0x554ad2e, v18
	v_mul_f32_e32 v18, v68, v50
	ds_bpermute_b32 v130, v133, v50
	s_waitcnt lgkmcnt(1)
	v_cndmask_b32_e64 v50, v53, v51, s[12:13]
	v_mul_f32_e32 v51, v42, v50
	v_cvt_pk_bf16_f32 v51, v51, s0
	ds_write_b16 v215, v51
	v_mul_f32_e32 v51, v43, v50
	v_cvt_pk_bf16_f32 v51, v51, s0
	ds_write_b16 v215, v51 offset:272
	v_mul_f32_e32 v51, v44, v50
	v_cvt_pk_bf16_f32 v51, v51, s0
	ds_write_b16 v219, v51
	v_mul_f32_e32 v51, v45, v50
	v_cvt_pk_bf16_f32 v51, v51, s0
	ds_write_b16 v219, v51 offset:272
	v_mul_f32_e32 v51, v38, v50
	v_cvt_pk_bf16_f32 v51, v51, s0
	ds_write_b16 v215, v51 offset:4352
	v_mul_f32_e32 v51, v39, v50
	v_cvt_pk_bf16_f32 v51, v51, s0
	v_rcp_f32_e32 v70, v55
	ds_write_b16 v215, v51 offset:4624
	v_mul_f32_e32 v51, v40, v50
	v_mul_f32_e32 v50, v41, v50
	v_cvt_pk_bf16_f32 v51, v51, s0
	v_cvt_pk_bf16_f32 v50, v50, s0
	v_cndmask_b32_e64 v69, 1.0, v52, s[4:5]
	ds_write_b16 v215, v51 offset:4896
	ds_write_b16 v215, v50 offset:5168
	v_mul_f32_e32 v50, v102, v59
	v_mul_f32_e32 v51, v103, v69
	v_mul_f32_e32 v50, v50, v68
	v_mul_f32_e32 v51, v51, v70
	v_med3_f32 v50, v50, s86, v214
	v_med3_f32 v51, v51, s86, v214
	v_rcp_f32_e32 v52, v50
	v_rcp_f32_e32 v53, v51
	v_mul_f32_e32 v58, v70, v54
	ds_bpermute_b32 v252, v133, v54
	v_pk_add_f32 v[54:55], v[102:103], 1.0 op_sel_hi:[1,0] neg_lo:[1,0] neg_hi:[1,0]
	v_add_u32_e32 v229, s81, v198
	v_pk_mul_f32 v[52:53], v[54:55], v[52:53]
	v_and_b32_e32 v55, 0xffff0000, v170
	v_cvt_pk_bf16_f32 v54, v52, v53
	ds_write_b32 v222, v54
	v_lshlrev_b32_e32 v54, 16, v170
	v_pk_mul_f32 v[50:51], v[50:51], v[54:55]
	v_add_u32_e32 v230, s61, v198
	v_cvt_pk_bf16_f32 v56, v50, v51
	v_mul_f32_e32 v50, v60, v59
	v_mul_f32_e32 v51, v61, v69
	v_mul_f32_e32 v50, v50, v68
	v_mul_f32_e32 v51, v51, v70
	v_med3_f32 v50, v50, s86, v214
	v_med3_f32 v51, v51, s86, v214
; DEV int ltid() { int t = threadIdx.x; asm volatile("" : "+v"(t)); return t; }
; DEV unsigned cvt_pk4_fp8(f32x4 v) { unsigned r = 0; r = __builtin_amdgcn_cvt_pk_fp8_f32(v[0], v[1], r, false); r = __builtin_amdgcn_cvt_pk_fp8_f32(v[2], v[3], r, true); return r; }
; DEV void fill_write(const f32x4 (&ld)[4], int bufsel) {
;   extern __shared__ __attribute__((aligned(16))) char shm[];
;   unsigned* T = (unsigned*)(shm + FILL_LDS_OFF + bufsel * FILL_TB); const int tid = ltid(), tx = tid & 15, ty = tid >> 4;
;   constexpr float WS = (float)(1 << FP8_WSCALE_LOG2_);
; #pragma unroll
;   for (int j = 0; j < 4; ++j) T[(4 * tx + j) * 33 + ty] = cvt_pk4_fp8((f32x4){ld[0][j] * WS, ld[1][j] * WS, ld[2][j] * WS, ld[3][j] * WS});
; }
	v_rcp_f32_e32 v54, v50
	v_rcp_f32_e32 v55, v51
	ds_write_b32 v224, v56
	v_pk_add_f32 v[56:57], v[100:101], 1.0 op_sel_hi:[1,0] neg_lo:[1,0] neg_hi:[1,0]
	v_add_u32_e32 v231, s81, v199
	v_pk_mul_f32 v[54:55], v[56:57], v[54:55]
	v_and_b32_e32 v57, 0xffff0000, v167
	v_cvt_pk_bf16_f32 v56, v54, v55
	ds_write_b32 v225, v56
	v_lshlrev_b32_e32 v56, 16, v167
	v_pk_mul_f32 v[50:51], v[50:51], v[56:57]
	v_mul_f32_e32 v48, v48, v59
	v_cvt_pk_bf16_f32 v50, v50, v51
	v_mov_b32_e32 v51, v54
	v_mov_b32_e32 v54, v53
	ds_write_b32 v226, v50
	v_mov_b32_e32 v50, v52
	v_pk_mul_f32 v[52:53], v[58:59], v[54:55] op_sel_hi:[0,1]
	v_mul_f32_e32 v54, v62, v59
	v_mul_f32_e32 v54, v54, v68
	v_med3_f32 v56, v54, s86, v214
	v_mul_f32_e32 v54, v63, v69
	v_mul_f32_e32 v54, v54, v70
	v_med3_f32 v57, v54, s86, v214
	v_rcp_f32_e32 v60, v56
	v_rcp_f32_e32 v61, v57
	v_cvt_pk_bf16_f32 v54, v52, v53
	v_pk_add_f32 v[52:53], v[98:99], 1.0 op_sel_hi:[1,0] neg_lo:[1,0] neg_hi:[1,0]
	v_pk_mul_f32 v[50:51], v[18:19], v[50:51] op_sel_hi:[0,1]
	v_pk_mul_f32 v[52:53], v[52:53], v[60:61]
	v_lshlrev_b32_e32 v60, 16, v163
	v_and_b32_e32 v61, 0xffff0000, v163
	v_mul_f32_e32 v55, v64, v59
	v_cvt_pk_bf16_f32 v50, v50, v51
	v_cvt_pk_bf16_f32 v51, v52, v53
	v_pk_mul_f32 v[56:57], v[56:57], v[60:61]
	v_mul_f32_e32 v55, v55, v68
	ds_write_b32 v227, v51
	v_cvt_pk_bf16_f32 v51, v56, v57
	v_med3_f32 v56, v55, s86, v214
	v_mul_f32_e32 v55, v65, v69
	v_mul_f32_e32 v55, v55, v70
	v_med3_f32 v57, v55, s86, v214
	v_rcp_f32_e32 v60, v56
	v_rcp_f32_e32 v61, v57
	v_pk_add_f32 v[62:63], v[96:97], 1.0 op_sel_hi:[1,0] neg_lo:[1,0] neg_hi:[1,0]
	ds_write_b32 v228, v51
	v_mul_f32_e32 v49, v49, v69
	v_pk_mul_f32 v[60:61], v[62:63], v[60:61]
	v_lshlrev_b32_e32 v62, 16, v161
	v_and_b32_e32 v63, 0xffff0000, v161
	v_cvt_pk_bf16_f32 v51, v60, v61
	v_pk_mul_f32 v[56:57], v[56:57], v[62:63]
	ds_write_b32 v229, v51
	v_cvt_pk_bf16_f32 v51, v56, v57
	ds_write_b32 v230, v51
	v_mul_f32_e32 v51, v66, v59
	v_mov_b32_e32 v57, v60
	v_mov_b32_e32 v60, v53
	v_mul_f32_e32 v51, v51, v68
	v_mov_b32_e32 v56, v52
	v_pk_mul_f32 v[52:53], v[58:59], v[60:61] op_sel_hi:[0,1]
	v_med3_f32 v60, v51, s86, v214
	v_mul_f32_e32 v51, v67, v69
	v_mul_f32_e32 v51, v51, v70
	v_med3_f32 v61, v51, s86, v214
	v_rcp_f32_e32 v62, v60
	v_rcp_f32_e32 v63, v61
	v_cvt_pk_bf16_f32 v55, v52, v53
	v_pk_add_f32 v[52:53], v[94:95], 1.0 op_sel_hi:[1,0] neg_lo:[1,0] neg_hi:[1,0]
	v_pk_mul_f32 v[56:57], v[18:19], v[56:57] op_sel_hi:[0,1]
	v_pk_mul_f32 v[52:53], v[52:53], v[62:63]
	v_cvt_pk_bf16_f32 v51, v56, v57
	v_cvt_pk_bf16_f32 v56, v52, v53
	ds_write_b32 v231, v56
	v_lshlrev_b32_e32 v56, 16, v160
	v_and_b32_e32 v57, 0xffff0000, v160
	v_mul_f32_e32 v48, v48, v68
	v_mul_f32_e32 v49, v49, v70
	v_pk_mul_f32 v[56:57], v[60:61], v[56:57]
	v_med3_f32 v48, v48, s86, v214
	v_med3_f32 v49, v49, s86, v214
	v_cvt_pk_bf16_f32 v60, v56, v57
	v_rcp_f32_e32 v56, v48
	v_rcp_f32_e32 v57, v49
	v_add_u32_e32 v232, s61, v199
	ds_write_b32 v232, v60
	v_pk_add_f32 v[60:61], v[92:93], 1.0 op_sel_hi:[1,0] neg_lo:[1,0] neg_hi:[1,0]
	v_add_u32_e32 v233, s81, v200
	v_pk_mul_f32 v[56:57], v[60:61], v[56:57]
	v_mul_f32_e32 v46, v46, v59
	v_cvt_pk_bf16_f32 v60, v56, v57
	v_mul_f32_e32 v47, v47, v69
	ds_write_b32 v233, v60
	v_lshlrev_b32_e32 v60, 16, v159
	v_and_b32_e32 v61, 0xffff0000, v159
	v_mul_f32_e32 v46, v46, v68
	v_mul_f32_e32 v47, v47, v70
	v_pk_mul_f32 v[48:49], v[48:49], v[60:61]
	v_med3_f32 v46, v46, s86, v214
	v_med3_f32 v47, v47, s86, v214
	v_cvt_pk_bf16_f32 v48, v48, v49
	v_add_u32_e32 v234, s61, v200
	v_rcp_f32_e32 v60, v46
	v_rcp_f32_e32 v61, v47
	ds_write_b32 v234, v48
	v_mov_b32_e32 v48, v52
	v_mov_b32_e32 v49, v56
	v_pk_mul_f32 v[48:49], v[18:19], v[48:49] op_sel_hi:[0,1]
	v_cvt_pk_bf16_f32 v52, v48, v49
	v_pk_add_f32 v[48:49], v[90:91], 1.0 op_sel_hi:[1,0] neg_lo:[1,0] neg_hi:[1,0]
	v_mul_f32_e32 v20, v20, v59
	v_mul_f32_e32 v21, v21, v69
	v_pk_mul_f32 v[48:49], v[48:49], v[60:61]
	v_lshlrev_b32_e32 v60, 16, v158
	v_and_b32_e32 v61, 0xffff0000, v158
	v_mul_f32_e32 v20, v20, v68
	v_mul_f32_e32 v21, v21, v70
	v_mov_b32_e32 v56, v53
	v_cvt_pk_bf16_f32 v53, v48, v49
	v_add_u32_e32 v235, s81, v201
	v_pk_mul_f32 v[46:47], v[46:47], v[60:61]
	v_med3_f32 v20, v20, s86, v214
	v_med3_f32 v21, v21, s86, v214
	ds_write_b32 v235, v53
	v_cvt_pk_bf16_f32 v53, v46, v47
	v_rcp_f32_e32 v46, v20
	v_rcp_f32_e32 v47, v21
	v_pk_add_f32 v[60:61], v[88:89], 1.0 op_sel_hi:[1,0] neg_lo:[1,0] neg_hi:[1,0]
	v_add_u32_e32 v236, s61, v201
	v_add_u32_e32 v238, s61, v202
	v_pk_mul_f32 v[46:47], v[60:61], v[46:47]
	v_lshlrev_b32_e32 v60, 16, v157
	v_and_b32_e32 v61, 0xffff0000, v157
	v_pk_mul_f32 v[20:21], v[20:21], v[60:61]
	ds_write_b32 v236, v53
	v_cvt_pk_bf16_f32 v20, v20, v21
	ds_write_b32 v238, v20
	v_mov_b32_e32 v20, v48
	v_mov_b32_e32 v21, v46
	v_cvt_pk_bf16_f32 v53, v46, v47
	v_add_u32_e32 v237, s81, v202
	v_pk_mul_f32 v[20:21], v[18:19], v[20:21] op_sel_hi:[0,1]
	ds_write_b32 v237, v53
	v_cvt_pk_bf16_f32 v53, v20, v21
	v_mul_f32_e32 v10, 0x42800000, v10
	v_mul_f32_e32 v14, 0x42800000, v14
	v_mov_b32_e32 v21, v19
	v_cvt_pk_fp8_f32 v21, v10, v14
	v_mul_f32_e32 v10, 0x42800000, v11
	v_mul_f32_e32 v11, 0x42800000, v15
	v_mov_b32_e32 v14, v19
	v_cvt_pk_fp8_f32 v14, v10, v11
; DEV int ltid() { int t = threadIdx.x; asm volatile("" : "+v"(t)); return t; }
; DEV unsigned cvt_pk4_fp8(f32x4 v) { unsigned r = 0; r = __builtin_amdgcn_cvt_pk_fp8_f32(v[0], v[1], r, false); r = __builtin_amdgcn_cvt_pk_fp8_f32(v[2], v[3], r, true); return r; }
; DEV void fill_load(CParams& p, int wg, int slot, f32x4 (&ld)[4]) {
;   const FillDesc d = fill_decode(p, wg, slot); const int tid = ltid(), tx = tid & 15, ty = tid >> 4;
;   const float* sp = d.src + (long)(d.kh + 4 * ty) * d.ldsrc + d.n0 + 4 * tx;
; #pragma unroll
;   for (int r = 0; r < 4; ++r) ld[r] = *(const f32x4*)(sp + (long)r * d.ldsrc);
; }
; DEV void fill_write(const f32x4 (&ld)[4], int bufsel) {
;   extern __shared__ __attribute__((aligned(16))) char shm[];
;   unsigned* T = (unsigned*)(shm + FILL_LDS_OFF + bufsel * FILL_TB); const int tid = ltid(), tx = tid & 15, ty = tid >> 4;
;   constexpr float WS = (float)(1 << FP8_WSCALE_LOG2_);
; #pragma unroll
;   for (int j = 0; j < 4; ++j) T[(4 * tx + j) * 33 + ty] = cvt_pk4_fp8((f32x4){ld[0][j] * WS, ld[1][j] * WS, ld[2][j] * WS, ld[3][j] * WS});
; }
; DEV void fill_store(CParams& p, int wg, int slot, int bufsel) {
;   extern __shared__ __attribute__((aligned(16))) char shm[];
;   const unsigned* T = (const unsigned*)(shm + FILL_LDS_OFF + bufsel * FILL_TB); const int tid = ltid(), nl = tid >> 3, cc = tid & 7;
;   const FillDesc d = fill_decode(p, wg, slot);
;   u32x4 v; v.x = T[nl * 33 + 4 * cc]; v.y = T[nl * 33 + 4 * cc + 1]; v.z = T[nl * 33 + 4 * cc + 2]; v.w = T[nl * 33 + 4 * cc + 3];
;   *(u32x4*)(d.dst + (long)perm_row(d.perm, d.n0 + nl) * 2048 + d.kh + 16 * cc) = v;
; }
	v_mul_f32_e32 v2, 0x42800000, v2
	v_mul_f32_e32 v6, 0x42800000, v6
	v_cvt_pk_fp8_f32 v21, v2, v6 op_sel:[0,0,1]
	v_mul_f32_e32 v2, 0x42800000, v3
	v_mul_f32_e32 v3, 0x42800000, v7
	v_cvt_pk_fp8_f32 v14, v2, v3 op_sel:[0,0,1]
	v_mul_f32_e32 v2, 0x42800000, v12
	v_mul_f32_e32 v3, 0x42800000, v16
	v_mov_b32_e32 v7, v19
	v_mul_f32_e32 v6, 0x42800000, v8
	v_cvt_pk_fp8_f32 v7, v2, v3
	v_mul_f32_e32 v2, 0x42800000, v13
	v_mul_f32_e32 v3, 0x42800000, v17
	v_mov_b32_e32 v8, v19
	v_mov_b32_e32 v46, v49
	v_cvt_pk_fp8_f32 v8, v2, v3
	v_pk_mul_f32 v[56:57], v[58:59], v[56:57] op_sel_hi:[0,1]
	v_pk_mul_f32 v[46:47], v[58:59], v[46:47] op_sel_hi:[0,1]
	v_mov_b32_e32 v18, v0
	v_cvt_pk_bf16_f32 v56, v56, v57
	v_cvt_pk_bf16_f32 v57, v46, v47
	ds_write_b128 v134, v[50:53]
	ds_write_b128 v135, v[54:57]
	v_mul_f32_e32 v4, 0x42800000, v4
	v_ashrrev_i32_e32 v20, 4, v18
	v_lshlrev_b32_e32 v18, 2, v18
	v_mul_f32_e32 v2, 0x42800000, v5
	v_mul_f32_e32 v3, 0x42800000, v9
	v_and_b32_e32 v18, 60, v18
	v_cvt_pk_fp8_f32 v7, v4, v6 op_sel:[0,0,1]
	v_cvt_pk_fp8_f32 v8, v2, v3 op_sel:[0,0,1]
	s_add_i32 s73, s83, 0xffffff00
	v_lshlrev_b32_e32 v20, 2, v20
	v_mul_u32_u24_e32 v2, 0x84, v18
	s_ashr_i32 s72, s73, 1
	v_add3_u32 v2, s78, v20, v2
	s_cmpk_gt_i32 s72, 0x3fff
	s_mov_b64 s[70:71], -1
	ds_write2_b32 v2, v21, v14 offset1:33
	ds_write2_b32 v2, v7, v8 offset0:66 offset1:99
	s_add_i32 s70, s83, 0xffffff00
	s_lshr_b32 s70, s70, 8
	s_lshl_b32 s70, s70, 23
	s_add_u32 s70, s64, s70
	s_addc_u32 s71, s65, 0
	s_add_u32 s70, s70, s98
	s_addc_u32 s71, s71, 0
	s_add_u32 s72, s70, 0x8000
	s_addc_u32 s73, s71, 0
	v_lshrrev_b32_e32 v2, 4, v0
	v_and_b32_e32 v3, 15, v0
	v_lshlrev_b32_e32 v2, 16, v2
	v_lshl_or_b32 v2, v3, 4, v2
	v_add_u32_e32 v3, 0x4000, v2
	v_add_u32_e32 v6, 0x4000, v2
	global_load_dwordx4 v[10:13], v2, s[70:71]
	global_load_dwordx4 v[14:17], v3, s[70:71]
	global_load_dwordx4 v[2:5], v2, s[72:73]
	s_nop 0
	global_load_dwordx4 v[6:9], v6, s[72:73]
	s_add_i32 s62, s89, 0x133f
	s_add_i32 s70, s90, 0x4c0
	s_and_b64 s[68:69], s[54:55], exec
	s_cselect_b32 s62, s70, s62
	s_sub_u32 s70, s62, 64
	s_lshl_b32 s72, s70, 11
	s_lshl_b32 s70, s70, 12
	s_add_u32 s70, s32, s70
	s_addc_u32 s71, s93, 0
	s_add_u32 s72, s94, s72
	s_addc_u32 s73, s95, 0
	s_waitcnt lgkmcnt(0)
	s_barrier
	v_add_u32_e32 v21, s78, v213
	ds_read2_b32 v[46:47], v21 offset1:1
	ds_read2_b32 v[48:49], v21 offset0:2 offset1:3
	v_lshrrev_b32_e32 v20, 1, v152
	global_load_dword v170, v20, s[72:73] offset:1024
	global_load_dwordx2 v[102:103], v152, s[70:71] offset:2048
	v_lshrrev_b32_e32 v21, 1, v136
	global_load_dword v167, v21, s[72:73] offset:1024
	global_load_dwordx2 v[100:101], v136, s[70:71] offset:2048
	v_lshrrev_b32_e32 v20, 1, v137
	global_load_dword v163, v20, s[72:73] offset:1024
	global_load_dwordx2 v[98:99], v137, s[70:71] offset:2048
	v_lshrrev_b32_e32 v21, 1, v138
	global_load_dword v161, v21, s[72:73] offset:1024
	global_load_dwordx2 v[96:97], v138, s[70:71] offset:2048
	v_lshrrev_b32_e32 v20, 1, v139
	global_load_dword v160, v20, s[72:73] offset:1024
	global_load_dwordx2 v[94:95], v139, s[70:71] offset:2048
	v_lshrrev_b32_e32 v21, 1, v140
	global_load_dword v159, v21, s[72:73] offset:1024
	global_load_dwordx2 v[92:93], v140, s[70:71] offset:2048
	v_lshrrev_b32_e32 v20, 1, v142
	global_load_dword v158, v20, s[72:73] offset:1024
	global_load_dwordx2 v[90:91], v142, s[70:71] offset:2048
	v_lshrrev_b32_e32 v21, 1, v144
	global_load_dword v157, v21, s[72:73] offset:1024
	global_load_dwordx2 v[88:89], v144, s[70:71] offset:2048
	s_sub_u32 s70, s62, 64
	s_lshl_b32 s70, s70, 11
	s_add_u32 s70, s96, s70
	s_addc_u32 s71, s97, 0
	global_load_dwordx2 v[104:105], v145, s[70:71] offset:1024
	s_add_i32 s92, s83, 0xfffffd00
	s_lshr_b32 s70, s92, 8
	s_lshr_b32 s71, s70, 2
	s_lshl_b32 s71, s71, 23
	s_and_b32 s70, s70, 3
	s_lshl_b32 s70, s70, 9
	s_or_b32 s70, s70, s71
	s_add_u32 s72, s44, s70
	s_addc_u32 s73, s45, 0
	s_waitcnt lgkmcnt(0)
	global_store_dwordx4 v212, v[46:49], s[72:73]
	v_add_u32_e32 v242, v206, v207
	v_add_u32_e32 v244, v206, v209
	v_add_u32_e32 v243, v206, v208
	ds_read_b128 v[58:61], v242
	ds_read_b128 v[54:57], v243
	v_add_u32_e32 v245, v206, v210
	ds_read_b128 v[50:53], v244
	ds_read_b128 v[46:49], v245
	v_mov_b32_e32 v62, 0
	v_mov_b32_e32 v66, 0
	v_mov_b32_e32 v67, 0
	v_mov_b32_e32 v68, 0
	v_mov_b32_e32 v69, 0
	s_and_saveexec_b64 s[68:69], s[16:17]
	s_cbranch_execz .LBB0_1018
	v_add_u32_e32 v18, v185, v184
	ds_read_b128 v[64:67], v18
	v_add_u32_e32 v18, v185, v183
	ds_read_b128 v[68:71], v18
	v_add_u32_e32 v18, v185, v182
	ds_read_b128 v[72:75], v18
	v_add_u32_e32 v18, v185, v181
	s_waitcnt lgkmcnt(2)
	v_mfma_f32_16x16x32_bf16 v[64:67], v[64:67], v[58:61], 0
	s_waitcnt lgkmcnt(1)
	v_mfma_f32_16x16x32_bf16 v[64:67], v[68:71], v[54:57], v[64:67]
	ds_read_b128 v[68:71], v18
	s_waitcnt lgkmcnt(1)
	v_mfma_f32_16x16x32_bf16 v[64:67], v[72:75], v[50:53], v[64:67]
	s_waitcnt lgkmcnt(0)
	v_mfma_f32_16x16x32_bf16 v[66:69], v[68:71], v[46:49], v[64:67]
	s_and_saveexec_b64 s[70:71], s[38:39]
	s_nop 6
	v_cndmask_b32_e64 v66, v66, 0, s[18:19]
	v_cndmask_b32_e64 v67, 0, v67, s[20:21]
	v_cndmask_b32_e64 v68, v68, 0, s[22:23]
	v_cndmask_b32_e64 v69, v69, 0, s[24:25]
	s_or_b64 exec, exec, s[70:71]

.LBB0_1034:
	s_or_b64 exec, exec, s[68:69]
	ds_read_b128 v[62:65], v162
	s_addk_i32 s89, 0x13bf
	s_addk_i32 s90, 0x440
	s_and_b64 s[68:69], s[54:55], exec
	s_cselect_b32 s62, s90, s89
	v_add_u32_e32 v20, s62, v187
	v_ashrrev_i32_e32 v21, 31, v20
	v_lshlrev_b64 v[20:21], 11, v[20:21]
	v_lshl_add_u64 v[20:21], v[110:111], 0, v[20:21]
	s_waitcnt lgkmcnt(0)
	v_mfma_f32_16x16x32_bf16 v[58:61], v[62:65], v[58:61], v[78:81]
	ds_read_b128 v[62:65], v162 offset:64
	v_cndmask_b32_e64 v18, v252, v130, s[12:13]
	v_pk_mul_f32 v[44:45], v[44:45], v[18:19] op_sel_hi:[1,0]
	v_pk_mul_f32 v[42:43], v[42:43], v[18:19] op_sel_hi:[1,0]
	v_pk_mul_f32 v[40:41], v[40:41], v[18:19] op_sel_hi:[1,0]
	v_pk_mul_f32 v[38:39], v[38:39], v[18:19] op_sel_hi:[1,0]
	v_add_u32_e32 v66, v186, v194
	v_add_u32_e32 v73, 0x4400, v156
	s_waitcnt lgkmcnt(0)
	v_mfma_f32_16x16x32_bf16 v[54:57], v[62:65], v[54:57], v[58:61]
	v_add_u32_e32 v65, v186, v193
	s_cmp_gt_u32 s57, 63
	s_nop 0
	ds_read_b128 v[58:61], v162 offset:128
	s_cselect_b64 s[68:69], -1, 0
	s_and_b64 vcc, exec, s[68:69]
	s_waitcnt lgkmcnt(0)
	v_mfma_f32_16x16x32_bf16 v[50:53], v[58:61], v[50:53], v[54:57]
	s_nop 2
	ds_read_b128 v[54:57], v162 offset:192
	s_waitcnt vmcnt(37)
	v_pk_mul_f32 v[58:59], v[124:125], v[126:127]
	s_waitcnt vmcnt(35)
	v_pk_mul_f32 v[60:61], v[122:123], v[58:59]
	s_waitcnt lgkmcnt(0)
	v_mfma_f32_16x16x32_bf16 v[46:49], v[54:57], v[46:49], v[50:53]
	s_nop 7
	v_cvt_pk_bf16_f32 v46, v46, v47
	v_cvt_pk_bf16_f32 v47, v48, v49
	global_store_dwordx2 v[20:21], v[46:47], off offset:1024
	ds_read_b128 v[46:49], v154
	ds_read_b128 v[50:53], v154 offset:64
	ds_read_b128 v[54:57], v153
	s_waitcnt lgkmcnt(0)
	v_mfma_f32_16x16x32_bf16 v[42:45], v[54:57], v[46:49], v[42:45]
	ds_read_b128 v[54:57], v153 offset:64
	s_waitcnt lgkmcnt(0)
	v_mfma_f32_16x16x32_bf16 v[42:45], v[54:57], v[50:53], v[42:45]
	ds_read_b128 v[54:57], v153 offset:2304
	s_waitcnt lgkmcnt(0)
	v_mfma_f32_16x16x32_bf16 v[38:41], v[54:57], v[46:49], v[38:41]
	ds_read_b128 v[46:49], v153 offset:2368
	s_waitcnt vmcnt(34)
	v_pk_mul_f32 v[54:55], v[120:121], v[60:61]
	s_waitcnt vmcnt(25)
	ds_write_b16 v146, v128 offset:53248
	ds_write_b16_d16_hi v146, v128 offset:53392
	ds_write_b16 v146, v129 offset:53536
	ds_write_b16_d16_hi v146, v129 offset:53680
	s_waitcnt lgkmcnt(4)
	v_mfma_f32_16x16x32_bf16 v[38:41], v[46:49], v[50:53], v[38:41]
	v_mul_f32_e64 v50, v118, v54
	v_mul_f32_e64 v51, v119, v55
	v_pk_mul_f32 v[48:49], v[50:51], v[116:117]
	s_nop 0
	v_pk_mul_f32 v[46:47], v[48:49], v[114:115]
	s_nop 0
	v_pk_mul_f32 v[20:21], v[46:47], v[112:113]
	ds_bpermute_b32 v52, v1, v20
	ds_bpermute_b32 v53, v1, v21
	s_waitcnt lgkmcnt(0)
	v_pk_mul_f32 v[52:53], v[20:21], v[52:53]
	s_nop 0
	v_cndmask_b32_e64 v53, v53, v21, s[6:7]
	v_cndmask_b32_e64 v52, v52, v20, s[6:7]
	ds_bpermute_b32 v56, v131, v52
	ds_bpermute_b32 v57, v131, v53
	s_waitcnt lgkmcnt(0)
	v_pk_mul_f32 v[56:57], v[52:53], v[56:57]
	s_nop 0
	v_cndmask_b32_e64 v53, v57, v53, s[8:9]
	v_cndmask_b32_e64 v52, v56, v52, s[8:9]
	ds_bpermute_b32 v56, v132, v52
	ds_bpermute_b32 v57, v132, v53
	s_waitcnt lgkmcnt(0)
	v_pk_mul_f32 v[56:57], v[52:53], v[56:57]
	s_nop 0
	v_cndmask_b32_e64 v52, v56, v52, s[10:11]
	v_cndmask_b32_e64 v18, v57, v53, s[10:11]
	ds_bpermute_b32 v53, v1, v52
	ds_bpermute_b32 v63, v151, v18
	ds_bpermute_b32 v56, v1, v18
	ds_bpermute_b32 v62, v150, v18
	s_waitcnt lgkmcnt(3)
	v_cndmask_b32_e64 v57, 1.0, v53, s[4:5]
	ds_bpermute_b32 v53, v150, v52
	ds_bpermute_b32 v52, v151, v52
	s_waitcnt lgkmcnt(3)
	v_cndmask_b32_e64 v69, 1.0, v56, s[4:5]
	s_waitcnt lgkmcnt(2)
	ds_bpermute_b32 v56, v133, v62
	v_mul_f32_e32 v58, v58, v57
	v_mul_f32_e32 v59, v59, v69
	s_waitcnt lgkmcnt(1)
	v_max_f32_e32 v18, v52, v52
	v_max_f32_e32 v18, 0x554ad2e, v18
	v_rcp_f32_e32 v68, v18
	v_max_f32_e32 v18, v63, v63
	ds_bpermute_b32 v52, v133, v52
	ds_bpermute_b32 v63, v133, v63
	v_max_f32_e32 v64, 0x554ad2e, v18
	v_rcp_f32_e32 v70, v64
	v_mul_f32_e32 v58, v58, v68
	v_med3_f32 v58, v58, s86, v214
	s_waitcnt lgkmcnt(0)
	v_cndmask_b32_e64 v52, v63, v52, s[12:13]
	v_mul_f32_e32 v63, v42, v52
	v_cvt_pk_bf16_f32 v63, v63, s0
	ds_write_b16 v65, v63 offset:57856
	v_mul_f32_e32 v63, v43, v52
	v_cvt_pk_bf16_f32 v63, v63, s0
	ds_write_b16 v65, v63 offset:58128
	v_mul_f32_e32 v63, v44, v52
	v_cvt_pk_bf16_f32 v63, v63, s0
	ds_write_b16 v66, v63 offset:57856
	v_mul_f32_e32 v63, v45, v52
	v_cvt_pk_bf16_f32 v63, v63, s0
	ds_write_b16 v66, v63 offset:58128
	v_mul_f32_e32 v63, v38, v52
	v_cvt_pk_bf16_f32 v63, v63, s0
	ds_write_b16 v65, v63 offset:62208
	v_mul_f32_e32 v63, v39, v52
	v_cvt_pk_bf16_f32 v63, v63, s0
	ds_write_b16 v65, v63 offset:62480
	v_mul_f32_e32 v63, v40, v52
	v_mul_f32_e32 v52, v41, v52
	v_cvt_pk_bf16_f32 v63, v63, s0
	v_cvt_pk_bf16_f32 v52, v52, s0
	ds_write_b16 v65, v63 offset:62752
	ds_write_b16 v65, v52 offset:63024
	v_mul_f32_e32 v52, v70, v62
	v_mul_f32_e32 v62, v126, v57
	v_mul_f32_e32 v63, v127, v69
	v_mul_f32_e32 v62, v62, v68
	v_mul_f32_e32 v63, v63, v70
	v_med3_f32 v62, v62, s86, v214
	v_med3_f32 v63, v63, s86, v214
	v_rcp_f32_e32 v64, v62
	v_rcp_f32_e32 v65, v63
	v_pk_add_f32 v[66:67], v[126:127], 1.0 op_sel_hi:[1,0] neg_lo:[1,0] neg_hi:[1,0]
	v_mul_f32_e32 v59, v59, v70
	v_med3_f32 v59, v59, s86, v214
	v_pk_mul_f32 v[64:65], v[66:67], v[64:65]
	v_lshlrev_b32_e32 v66, 16, v251
	v_and_b32_e32 v67, 0xffff0000, v251
	v_pk_mul_f32 v[62:63], v[62:63], v[66:67]
	v_pk_add_f32 v[66:67], v[124:125], 1.0 op_sel_hi:[1,0] neg_lo:[1,0] neg_hi:[1,0]
	v_cvt_pk_bf16_f32 v72, v62, v63
	v_rcp_f32_e32 v62, v58
	v_rcp_f32_e32 v63, v59
	v_cvt_pk_bf16_f32 v71, v64, v65
	v_mul_f32_e32 v18, v68, v53
	ds_bpermute_b32 v53, v133, v53
	v_pk_mul_f32 v[62:63], v[66:67], v[62:63]
	v_and_b32_e32 v67, 0xffff0000, v250
	v_cvt_pk_bf16_f32 v66, v62, v63
	ds_write2_b32 v73, v71, v66 offset1:68
	v_lshlrev_b32_e32 v66, 16, v250
	v_pk_mul_f32 v[58:59], v[58:59], v[66:67]
	v_pk_add_f32 v[66:67], v[122:123], 1.0 op_sel_hi:[1,0] neg_lo:[1,0] neg_hi:[1,0]
	v_cvt_pk_bf16_f32 v58, v58, v59
	ds_write2_b32 v156, v72, v58 offset1:68
	v_mov_b32_e32 v58, v64
	v_mov_b32_e32 v59, v62
	v_pk_mul_f32 v[58:59], v[18:19], v[58:59] op_sel_hi:[0,1]
	v_cvt_pk_bf16_f32 v58, v58, v59
	v_mul_f32_e32 v59, v60, v57
	v_mul_f32_e32 v59, v59, v68
	v_med3_f32 v60, v59, s86, v214
	v_mul_f32_e32 v59, v61, v69
	v_mul_f32_e32 v59, v59, v70
	v_med3_f32 v61, v59, s86, v214
	v_mov_b32_e32 v62, v65
	v_rcp_f32_e32 v64, v60
	v_rcp_f32_e32 v65, v61
	v_mul_f32_e32 v54, v54, v57
	v_mul_f32_e32 v55, v55, v69
	v_mul_f32_e32 v54, v54, v68
	v_pk_mul_f32 v[64:65], v[66:67], v[64:65]
	v_lshlrev_b32_e32 v66, 16, v249
	v_and_b32_e32 v67, 0xffff0000, v249
	v_mul_f32_e32 v55, v55, v70
	s_waitcnt lgkmcnt(2)
; DEV int ltid() { int t = threadIdx.x; asm volatile("" : "+v"(t)); return t; }
; DEV unsigned cvt_pk4_fp8(f32x4 v) { unsigned r = 0; r = __builtin_amdgcn_cvt_pk_fp8_f32(v[0], v[1], r, false); r = __builtin_amdgcn_cvt_pk_fp8_f32(v[2], v[3], r, true); return r; }
; DEV void fill_load(CParams& p, int wg, int slot, f32x4 (&ld)[4]) {
;   const FillDesc d = fill_decode(p, wg, slot); const int tid = ltid(), tx = tid & 15, ty = tid >> 4;
;   const float* sp = d.src + (long)(d.kh + 4 * ty) * d.ldsrc + d.n0 + 4 * tx;
; #pragma unroll
;   for (int r = 0; r < 4; ++r) ld[r] = *(const f32x4*)(sp + (long)r * d.ldsrc);
; }
; DEV void fill_write(const f32x4 (&ld)[4], int bufsel) {
;   extern __shared__ __attribute__((aligned(16))) char shm[];
;   unsigned* T = (unsigned*)(shm + FILL_LDS_OFF + bufsel * FILL_TB); const int tid = ltid(), tx = tid & 15, ty = tid >> 4;
;   constexpr float WS = (float)(1 << FP8_WSCALE_LOG2_);
; #pragma unroll
;   for (int j = 0; j < 4; ++j) T[(4 * tx + j) * 33 + ty] = cvt_pk4_fp8((f32x4){ld[0][j] * WS, ld[1][j] * WS, ld[2][j] * WS, ld[3][j] * WS});
; }
	v_pk_mul_f32 v[62:63], v[52:53], v[62:63] op_sel_hi:[0,1]
	v_pk_mul_f32 v[60:61], v[60:61], v[66:67]
	v_med3_f32 v54, v54, s86, v214
	v_med3_f32 v55, v55, s86, v214
	v_cvt_pk_bf16_f32 v62, v62, v63
	v_cvt_pk_bf16_f32 v63, v60, v61
	v_rcp_f32_e32 v60, v54
	v_rcp_f32_e32 v61, v55
	v_pk_add_f32 v[66:67], v[120:121], 1.0 op_sel_hi:[1,0] neg_lo:[1,0] neg_hi:[1,0]
	v_cvt_pk_bf16_f32 v59, v64, v65
	v_mul_f32_e32 v50, v50, v57
	v_pk_mul_f32 v[60:61], v[66:67], v[60:61]
	v_and_b32_e32 v67, 0xffff0000, v248
	v_cvt_pk_bf16_f32 v66, v60, v61
	ds_write2_b32 v73, v59, v66 offset0:136 offset1:204
	v_lshlrev_b32_e32 v66, 16, v248
	v_pk_mul_f32 v[54:55], v[54:55], v[66:67]
	v_mul_f32_e32 v51, v51, v69
	v_cvt_pk_bf16_f32 v54, v54, v55
	ds_write2_b32 v156, v63, v54 offset0:136 offset1:204
	v_mov_b32_e32 v54, v64
	v_mov_b32_e32 v55, v60
	v_mul_f32_e32 v50, v50, v68
	v_mul_f32_e32 v51, v51, v70
	v_pk_mul_f32 v[54:55], v[18:19], v[54:55] op_sel_hi:[0,1]
	v_med3_f32 v50, v50, s86, v214
	v_med3_f32 v51, v51, s86, v214
	v_cvt_pk_bf16_f32 v59, v54, v55
	v_rcp_f32_e32 v54, v50
	v_rcp_f32_e32 v55, v51
	v_mov_b32_e32 v60, v65
	v_pk_mul_f32 v[60:61], v[52:53], v[60:61] op_sel_hi:[0,1]
	v_cvt_pk_bf16_f32 v63, v60, v61
	v_pk_add_f32 v[60:61], v[118:119], 1.0 op_sel_hi:[1,0] neg_lo:[1,0] neg_hi:[1,0]
	v_mul_f32_e32 v48, v48, v57
	v_mul_f32_e32 v49, v49, v69
	v_pk_mul_f32 v[54:55], v[60:61], v[54:55]
	v_lshlrev_b32_e32 v60, 16, v247
	v_and_b32_e32 v61, 0xffff0000, v247
	v_mul_f32_e32 v48, v48, v68
	v_mul_f32_e32 v49, v49, v70
	v_pk_mul_f32 v[50:51], v[50:51], v[60:61]
	v_med3_f32 v48, v48, s86, v214
	v_med3_f32 v49, v49, s86, v214
	v_cvt_pk_bf16_f32 v65, v50, v51
	v_rcp_f32_e32 v50, v48
	v_rcp_f32_e32 v51, v49
	v_pk_add_f32 v[60:61], v[116:117], 1.0 op_sel_hi:[1,0] neg_lo:[1,0] neg_hi:[1,0]
	v_cvt_pk_bf16_f32 v64, v54, v55
	v_add_u32_e32 v66, 0x4800, v156
	v_pk_mul_f32 v[50:51], v[60:61], v[50:51]
	v_and_b32_e32 v61, 0xffff0000, v246
	v_cvt_pk_bf16_f32 v60, v50, v51
	ds_write2_b32 v66, v64, v60 offset0:16 offset1:84
	v_lshlrev_b32_e32 v60, 16, v246
	v_pk_mul_f32 v[48:49], v[48:49], v[60:61]
	v_add_u32_e32 v61, 0x400, v156
	v_cvt_pk_bf16_f32 v48, v48, v49
	v_mul_f32_e32 v46, v46, v57
	v_mul_f32_e32 v47, v47, v69
	ds_write2_b32 v61, v65, v48 offset0:16 offset1:84
	v_mov_b32_e32 v48, v54
	v_mov_b32_e32 v49, v50
	v_mul_f32_e32 v46, v46, v68
	v_mul_f32_e32 v47, v47, v70
	v_pk_mul_f32 v[48:49], v[18:19], v[48:49] op_sel_hi:[0,1]
	v_med3_f32 v46, v46, s86, v214
	v_med3_f32 v47, v47, s86, v214
	v_cvt_pk_bf16_f32 v60, v48, v49
	v_rcp_f32_e32 v48, v46
	v_rcp_f32_e32 v49, v47
	v_mov_b32_e32 v50, v55
	v_pk_mul_f32 v[50:51], v[52:53], v[50:51] op_sel_hi:[0,1]
	v_cvt_pk_bf16_f32 v64, v50, v51
	v_pk_add_f32 v[50:51], v[114:115], 1.0 op_sel_hi:[1,0] neg_lo:[1,0] neg_hi:[1,0]
	v_mul_f32_e32 v20, v20, v57
	v_mul_f32_e32 v21, v21, v69
	v_pk_mul_f32 v[48:49], v[50:51], v[48:49]
	v_lshlrev_b32_e32 v50, 16, v241
	v_and_b32_e32 v51, 0xffff0000, v241
	v_mul_f32_e32 v20, v20, v68
	v_mul_f32_e32 v21, v21, v70
	v_pk_mul_f32 v[46:47], v[46:47], v[50:51]
	v_med3_f32 v20, v20, s86, v214
	v_med3_f32 v21, v21, s86, v214
	v_cvt_pk_bf16_f32 v55, v46, v47
	v_rcp_f32_e32 v46, v20
	v_rcp_f32_e32 v47, v21
	v_pk_add_f32 v[50:51], v[112:113], 1.0 op_sel_hi:[1,0] neg_lo:[1,0] neg_hi:[1,0]
	v_cvt_pk_bf16_f32 v54, v48, v49
	v_pk_mul_f32 v[46:47], v[50:51], v[46:47]
	s_nop 0
	v_cvt_pk_bf16_f32 v50, v46, v47
	ds_write2_b32 v66, v54, v50 offset0:152 offset1:220
	v_lshlrev_b32_e32 v50, 16, v239
	v_and_b32_e32 v51, 0xffff0000, v239
	v_pk_mul_f32 v[20:21], v[20:21], v[50:51]
	s_nop 0
	v_cvt_pk_bf16_f32 v20, v20, v21
	ds_write2_b32 v61, v55, v20 offset0:152 offset1:220
	v_mov_b32_e32 v20, v48
	v_mov_b32_e32 v21, v46
	v_mov_b32_e32 v46, v49
	v_pk_mul_f32 v[20:21], v[18:19], v[20:21] op_sel_hi:[0,1]
	v_pk_mul_f32 v[46:47], v[52:53], v[46:47] op_sel_hi:[0,1]
	v_cvt_pk_bf16_f32 v61, v20, v21
	v_cvt_pk_bf16_f32 v65, v46, v47
	v_mov_b32_e32 v18, v0
	v_mul_f32_e32 v21, 0x42800000, v22
	v_mul_f32_e32 v46, 0x42800000, v26
	v_mov_b32_e32 v49, v19
	ds_write_b128 v147, v[58:61] offset:34816
	ds_write_b128 v148, v[62:65] offset:34816
	v_cvt_pk_fp8_f32 v49, v21, v46
	v_ashrrev_i32_e32 v20, 4, v18
	v_lshlrev_b32_e32 v18, 2, v18
	v_and_b32_e32 v18, 60, v18
	v_lshlrev_b32_e32 v20, 2, v20
	v_mul_f32_e32 v47, 0x42800000, v30
	v_mul_f32_e32 v48, 0x42800000, v34
	v_mul_u32_u24_e32 v18, 0x84, v18
	v_cvt_pk_fp8_f32 v49, v47, v48 op_sel:[0,0,1]
	v_add3_u32 v18, s82, v20, v18
	v_mul_f32_e32 v20, 0x42800000, v23
	v_mul_f32_e32 v21, 0x42800000, v27
	v_mov_b32_e32 v48, v19
	v_cvt_pk_fp8_f32 v48, v20, v21
	v_mul_f32_e32 v46, 0x42800000, v31
	v_mul_f32_e32 v47, 0x42800000, v35
	v_mul_f32_e32 v20, 0x42800000, v24
	v_cvt_pk_fp8_f32 v48, v46, v47 op_sel:[0,0,1]
	v_mul_f32_e32 v21, 0x42800000, v28
	v_mul_f32_e32 v46, 0x42800000, v32
	v_mul_f32_e32 v47, 0x42800000, v36
	ds_write2_b32 v18, v49, v48 offset1:33
	v_mov_b32_e32 v48, v19
	v_cvt_pk_fp8_f32 v48, v20, v21
	v_mul_f32_e32 v20, 0x42800000, v25
	v_mul_f32_e32 v21, 0x42800000, v29
	v_mov_b32_e32 v49, v19
	v_cvt_pk_fp8_f32 v49, v20, v21
	v_cvt_pk_fp8_f32 v48, v46, v47 op_sel:[0,0,1]
	v_mul_f32_e32 v46, 0x42800000, v33
	v_mul_f32_e32 v47, 0x42800000, v37
	v_cvt_pk_fp8_f32 v49, v46, v47 op_sel:[0,0,1]
	ds_write2_b32 v18, v48, v49 offset0:66 offset1:99
	s_cbranch_vccnz .LBB0_974
	s_lshr_b32 s70, s83, 8
	s_lshl_b32 s70, s70, 23
	s_add_u32 s70, s64, s70
	s_addc_u32 s71, s65, 0
	s_add_u32 s70, s70, s98
	s_addc_u32 s71, s71, 0
	s_add_u32 s72, s70, 0x8000
	s_addc_u32 s73, s71, 0
	v_lshrrev_b32_e32 v20, 4, v0
	v_and_b32_e32 v21, 15, v0
	v_lshlrev_b32_e32 v20, 16, v20
	v_lshl_or_b32 v20, v21, 4, v20
	v_add_u32_e32 v21, 0x4000, v20
	global_load_dwordx4 v[22:25], v20, s[70:71]
	global_load_dwordx4 v[26:29], v21, s[70:71]
	global_load_dwordx4 v[30:33], v20, s[72:73]
	s_nop 0
	global_load_dwordx4 v[34:37], v21, s[72:73]
	s_branch .LBB0_974

; __global__ void __launch_bounds__(NT, 2) k_mega(Params p) {
	.amdhsa_kernel _Z6k_mega6Params
		.amdhsa_group_segment_fixed_size 0
		.amdhsa_private_segment_fixed_size 0
		.amdhsa_kernarg_size 744
		.amdhsa_user_sgpr_count 2
		.amdhsa_user_sgpr_dispatch_ptr 0
		.amdhsa_user_sgpr_queue_ptr 0
		.amdhsa_user_sgpr_kernarg_segment_ptr 1
		.amdhsa_user_sgpr_dispatch_id 0
		.amdhsa_user_sgpr_kernarg_preload_length 0
		.amdhsa_user_sgpr_kernarg_preload_offset 0
		.amdhsa_user_sgpr_private_segment_size 0
		.amdhsa_uses_dynamic_stack 0
		.amdhsa_enable_private_segment 0
		.amdhsa_system_sgpr_workgroup_id_x 1
		.amdhsa_system_sgpr_workgroup_id_y 0
		.amdhsa_system_sgpr_workgroup_id_z 0
		.amdhsa_system_sgpr_workgroup_info 0
		.amdhsa_system_vgpr_workitem_id 0
		.amdhsa_next_free_vgpr 256
		.amdhsa_next_free_sgpr 99
		.amdhsa_accum_offset 256
		.amdhsa_reserve_vcc 1
		.amdhsa_float_round_mode_32 0
		.amdhsa_float_round_mode_16_64 0
		.amdhsa_float_denorm_mode_32 3
		.amdhsa_float_denorm_mode_16_64 3
		.amdhsa_dx10_clamp 1
		.amdhsa_ieee_mode 1
		.amdhsa_fp16_overflow 0
		.amdhsa_tg_split 0
		.amdhsa_exception_fp_ieee_invalid_op 0
		.amdhsa_exception_fp_denorm_src 0
		.amdhsa_exception_fp_ieee_div_zero 0
		.amdhsa_exception_fp_ieee_overflow 0
		.amdhsa_exception_fp_ieee_underflow 0
		.amdhsa_exception_fp_ieee_inexact 0
		.amdhsa_exception_int_div_zero 0
	.end_amdhsa_kernel

; __global__ void __launch_bounds__(NT, 2) k_mega(Params p) {
amdhsa.kernels:
  - .agpr_count:     0
    .args:
      - .offset:         0
        .size:           488
        .value_kind:     by_value
      - .offset:         488
        .size:           4
        .value_kind:     hidden_block_count_x
      - .offset:         492
        .size:           4
        .value_kind:     hidden_block_count_y
      - .offset:         496
        .size:           4
        .value_kind:     hidden_block_count_z
      - .offset:         500
        .size:           2
        .value_kind:     hidden_group_size_x
      - .offset:         502
        .size:           2
        .value_kind:     hidden_group_size_y
      - .offset:         504
        .size:           2
        .value_kind:     hidden_group_size_z
      - .offset:         506
        .size:           2
        .value_kind:     hidden_remainder_x
      - .offset:         508
        .size:           2
        .value_kind:     hidden_remainder_y
      - .offset:         510
        .size:           2
        .value_kind:     hidden_remainder_z
      - .offset:         528
        .size:           8
        .value_kind:     hidden_global_offset_x
      - .offset:         536
        .size:           8
        .value_kind:     hidden_global_offset_y
      - .offset:         544
        .size:           8
        .value_kind:     hidden_global_offset_z
      - .offset:         552
        .size:           2
        .value_kind:     hidden_grid_dims
      - .offset:         608
        .size:           4
        .value_kind:     hidden_dynamic_lds_size
    .group_segment_fixed_size: 0
    .kernarg_segment_align: 8
    .kernarg_segment_size: 744
    .language:       OpenCL C
    .language_version:
      - 2
      - 0
    .max_flat_workgroup_size: 512
    .name:           _Z6k_mega6Params
    .private_segment_fixed_size: 0
    .sgpr_count:     105
    .sgpr_spill_count: 0
    .symbol:         _Z6k_mega6Params.kd
    .uniform_work_group_size: 1
    .uses_dynamic_stack: false
    .vgpr_count:     256
    .vgpr_spill_count: 0
    .wavefront_size: 64
